# speedup vs baseline: 1.0892x; 1.0080x over previous
.LBB2_24:
	s_or_b64 exec, exec, s[0:1]
	v_and_b32_e32 v1, 31, v0
	v_lshlrev_b32_e32 v2, 2, v1
	v_lshl_or_b32 v2, s10, 7, v2
	v_or_b32_e32 v2, 0x1ee00, v2
	v_lshrrev_b32_e32 v158, 5, v156
	s_waitcnt lgkmcnt(0)
	s_barrier
	v_lshlrev_b32_e32 v250, 4, v158
	v_lshl_or_b32 v250, s10, 7, v250
	v_or_b32_e32 v254, 0x1ee00, v250
	ds_read_b128 v[168:171], v254 offset:0
	ds_read_b128 v[172:175], v254 offset:32
	ds_read_b128 v[176:179], v254 offset:64
	ds_read_b128 v[180:183], v254 offset:96
	v_bfe_u32 v255, v156, 2, 2
	v_lshl_add_u32 v250, v255, 2, v250
	v_add_u32_e32 v250, 0x1e400, v250
	s_waitcnt lgkmcnt(0)
	s_barrier
	ds_read_b32 v157, v2
	v_mul_u32_u24_e32 v2, 0x88, v1
	s_mul_i32 s0, s11, 0x4400
	v_lshlrev_b32_e32 v2, 1, v2
	v_lshlrev_b32_e32 v3, 4, v158
	v_mov_b32_e32 v138, v0
	v_add3_u32 v159, s0, v2, v3
	ds_read_b128 v[2:5], v159
	ds_read_b128 v[18:21], v159 offset:8704
	ds_read_b128 v[130:133], v159 offset:32
	s_waitcnt vmcnt(10) lgkmcnt(2)
	v_mfma_f32_32x32x16_f16 v[50:65], v[2:5], v[126:129], 0
	s_mov_b32 s4, 0xc060c00
	s_mov_b32 s5, 0xe400
	s_mulk_i32 s11, 0x2400
	s_lshl_b32 s0, s10, 6
	s_or_b32 s0, s11, s0
	s_add_i32 s0, s0, 0x11000
	v_mul_u32_u24_e32 v251, 0x90, v1
	v_lshl_add_u32 v251, v158, 3, v251
	v_add_u32_e32 v251, s0, v251
	s_waitcnt lgkmcnt(1)
	v_mfma_f32_32x32x16_f16 v[34:49], v[18:21], v[126:129], 0
	s_or_b32 s0, s8, 2
	s_ashr_i32 s1, s0, 31
	s_lshl_b64 s[0:1], s[0:1], 12
	s_add_u32 s0, s2, s0
	s_addc_u32 s1, s3, s1
	v_cmp_gt_u32_e32 vcc, 32, v156
	v_mfma_f32_32x32x16_f16 v[2:17], v[122:125], v[2:5], v[168:183]
	v_mfma_f32_32x32x16_f16 v[18:33], v[122:125], v[18:21], v[168:183]
	ds_read_b128 v[134:137], v159 offset:8736
	ds_read_b128 v[160:163], v159 offset:64
	s_waitcnt vmcnt(8) lgkmcnt(2)
	v_mfma_f32_32x32x16_f16 v[50:65], v[130:133], v[118:121], v[50:65]
	s_waitcnt lgkmcnt(1)
	v_mfma_f32_32x32x16_f16 v[34:49], v[134:137], v[118:121], v[34:49]
	v_mfma_f32_32x32x16_f16 v[2:17], v[114:117], v[130:133], v[2:17]
	v_mfma_f32_32x32x16_f16 v[18:33], v[114:117], v[134:137], v[18:33]
	ds_read_b128 v[130:133], v159 offset:8768
	ds_read_b128 v[134:137], v159 offset:96
	s_waitcnt vmcnt(6) lgkmcnt(2)
	v_mfma_f32_32x32x16_f16 v[50:65], v[160:163], v[110:113], v[50:65]
	s_waitcnt lgkmcnt(1)
	v_mfma_f32_32x32x16_f16 v[34:49], v[130:133], v[110:113], v[34:49]
	v_mfma_f32_32x32x16_f16 v[2:17], v[106:109], v[160:163], v[2:17]
	v_mfma_f32_32x32x16_f16 v[18:33], v[106:109], v[130:133], v[18:33]
	ds_read_b128 v[130:133], v159 offset:8800
	ds_read_b128 v[160:163], v159 offset:128
	s_waitcnt vmcnt(4) lgkmcnt(2)
	v_mfma_f32_32x32x16_f16 v[50:65], v[134:137], v[102:105], v[50:65]
	s_waitcnt lgkmcnt(1)
	v_mfma_f32_32x32x16_f16 v[34:49], v[130:133], v[102:105], v[34:49]
	v_mfma_f32_32x32x16_f16 v[2:17], v[98:101], v[134:137], v[2:17]
	v_mfma_f32_32x32x16_f16 v[18:33], v[98:101], v[130:133], v[18:33]
	ds_read_b128 v[130:133], v159 offset:8832
	ds_read_b128 v[134:137], v159 offset:160
	s_waitcnt vmcnt(3) lgkmcnt(2)
	v_mfma_f32_32x32x16_f16 v[50:65], v[160:163], v[94:97], v[50:65]
	s_waitcnt lgkmcnt(1)
	v_mfma_f32_32x32x16_f16 v[34:49], v[130:133], v[94:97], v[34:49]
	v_mfma_f32_32x32x16_f16 v[2:17], v[86:89], v[160:163], v[2:17]
	v_mfma_f32_32x32x16_f16 v[18:33], v[86:89], v[130:133], v[18:33]
	ds_read_b128 v[130:133], v159 offset:8864
	ds_read_b128 v[160:163], v159 offset:192
	s_waitcnt vmcnt(2) lgkmcnt(2)
	v_mfma_f32_32x32x16_f16 v[50:65], v[134:137], v[90:93], v[50:65]
	s_waitcnt lgkmcnt(1)
	v_mfma_f32_32x32x16_f16 v[34:49], v[130:133], v[90:93], v[34:49]
	v_mfma_f32_32x32x16_f16 v[2:17], v[78:81], v[134:137], v[2:17]
	v_mfma_f32_32x32x16_f16 v[18:33], v[78:81], v[130:133], v[18:33]
	ds_read_b128 v[130:133], v159 offset:8896
	ds_read_b128 v[164:167], v159 offset:224
	s_waitcnt vmcnt(1) lgkmcnt(2)
	v_mfma_f32_32x32x16_f16 v[50:65], v[160:163], v[82:85], v[50:65]
	s_waitcnt lgkmcnt(1)
	v_mfma_f32_32x32x16_f16 v[34:49], v[130:133], v[82:85], v[34:49]
	v_mfma_f32_32x32x16_f16 v[2:17], v[70:73], v[160:163], v[2:17]
	v_mfma_f32_32x32x16_f16 v[18:33], v[70:73], v[130:133], v[18:33]
	v_lshlrev_b32_e32 v130, 3, v138
	v_and_b32_e32 v241, 0x1f8, v130
	global_load_dwordx2 v[138:139], v241, s[0:1]
	global_load_dwordx2 v[134:135], v241, s[0:1] offset:512
	global_load_dwordx2 v[132:133], v241, s[0:1] offset:1024
	global_load_dwordx2 v[130:131], v241, s[0:1] offset:1536
	global_load_dwordx2 v[136:137], v241, s[0:1] offset:2048
	s_waitcnt vmcnt(5) lgkmcnt(0)
	v_mfma_f32_32x32x16_f16 v[50:65], v[164:167], v[74:77], v[50:65]
	v_mfma_f32_32x32x16_f16 v[2:17], v[66:69], v[164:167], v[2:17]
	s_nop 10
	v_cvt_pk_f16_f32 v57, v56, v57
	v_cvt_pk_f16_f32 v56, v54, v55
	v_cvt_pk_f16_f32 v55, v52, v53
	v_cvt_pk_f16_f32 v54, v50, v51
	v_perm_b32 v50, v240, v154, s42
	v_perm_b32 v51, v240, v154, s43
	v_perm_b32 v52, v240, v155, s42
	v_perm_b32 v53, v240, v155, s43
	v_pk_add_f16 v50, v50, s5 op_sel_hi:[1,0]
	v_pk_add_f16 v51, v51, s5 op_sel_hi:[1,0]
	v_pk_add_f16 v52, v52, s5 op_sel_hi:[1,0]
	v_pk_add_f16 v53, v53, s5 op_sel_hi:[1,0]
	v_cvt_pk_f16_f32 v65, v64, v65
	v_cvt_pk_f16_f32 v64, v62, v63
	v_cvt_pk_f16_f32 v63, v60, v61
	v_cvt_pk_f16_f32 v62, v58, v59
	v_mfma_f32_32x32x16_f16 v[2:17], v[54:57], v[50:53], v[2:17]
	v_perm_b32 v58, v240, v150, s42
	v_perm_b32 v59, v240, v150, s43
	v_perm_b32 v60, v240, v151, s42
	v_perm_b32 v61, v240, v151, s43
	v_pk_add_f16 v58, v58, s5 op_sel_hi:[1,0]
	v_pk_add_f16 v59, v59, s5 op_sel_hi:[1,0]
	v_pk_add_f16 v60, v60, s5 op_sel_hi:[1,0]
	v_pk_add_f16 v61, v61, s5 op_sel_hi:[1,0]
	s_nop 1
	v_mfma_f32_32x32x16_f16 v[2:17], v[62:65], v[58:61], v[2:17]
	ds_read_b128 v[160:163], v159 offset:8928
	v_perm_b32 v155, v240, v152, s43
	v_perm_b32 v164, v240, v153, s42
	s_waitcnt lgkmcnt(0)
	v_mfma_f32_32x32x16_f16 v[18:33], v[66:69], v[160:163], v[18:33]
	v_perm_b32 v154, v240, v152, s42
	v_perm_b32 v165, v240, v153, s43
	v_pk_add_f16 v152, v154, s5 op_sel_hi:[1,0]
	v_pk_add_f16 v153, v155, s5 op_sel_hi:[1,0]
	v_pk_add_f16 v154, v164, s5 op_sel_hi:[1,0]
	v_pk_add_f16 v155, v165, s5 op_sel_hi:[1,0]
	v_mfma_f32_32x32x16_f16 v[34:49], v[160:163], v[74:77], v[34:49]
	v_perm_b32 v151, v240, v148, s43
	v_perm_b32 v164, v240, v149, s42
	v_mfma_f32_32x32x16_f16 v[18:33], v[54:57], v[152:155], v[18:33]
	v_perm_b32 v150, v240, v148, s42
	v_perm_b32 v165, v240, v149, s43
	v_pk_add_f16 v148, v150, s5 op_sel_hi:[1,0]
	v_pk_add_f16 v149, v151, s5 op_sel_hi:[1,0]
	v_pk_add_f16 v150, v164, s5 op_sel_hi:[1,0]
	v_pk_add_f16 v151, v165, s5 op_sel_hi:[1,0]
	s_nop 2
	v_cvt_pk_f16_f32 v41, v40, v41
	v_cvt_pk_f16_f32 v40, v38, v39
	v_cvt_pk_f16_f32 v38, v34, v35
	v_cvt_pk_f16_f32 v39, v36, v37
	v_mfma_f32_32x32x16_f16 v[18:33], v[62:65], v[148:151], v[18:33]
	v_perm_b32 v34, v240, v146, s42
	v_perm_b32 v35, v240, v146, s43
	v_perm_b32 v36, v240, v147, s42
	v_perm_b32 v37, v240, v147, s43
	v_pk_add_f16 v34, v34, s5 op_sel_hi:[1,0]
	v_pk_add_f16 v35, v35, s5 op_sel_hi:[1,0]
	v_pk_add_f16 v36, v36, s5 op_sel_hi:[1,0]
	v_pk_add_f16 v37, v37, s5 op_sel_hi:[1,0]
	v_perm_b32 v146, v240, v144, s42
	v_perm_b32 v144, v240, v144, s43
	v_perm_b32 v147, v240, v145, s42
	v_perm_b32 v53, v240, v145, s43
	v_pk_add_f16 v50, v146, s5 op_sel_hi:[1,0]
	v_pk_add_f16 v51, v144, s5 op_sel_hi:[1,0]
	v_pk_add_f16 v52, v147, s5 op_sel_hi:[1,0]
	v_pk_add_f16 v53, v53, s5 op_sel_hi:[1,0]
	v_cvt_pk_f16_f32 v49, v48, v49
	v_cvt_pk_f16_f32 v48, v46, v47
	v_cvt_pk_f16_f32 v47, v44, v45
	v_mfma_f32_32x32x16_f16 v[2:17], v[38:41], v[34:37], v[2:17]
	v_cvt_pk_f16_f32 v46, v42, v43
	v_mfma_f32_32x32x16_f16 v[18:33], v[38:41], v[50:53], v[18:33]
	v_perm_b32 v34, v240, v140, s42
	v_perm_b32 v35, v240, v140, s43
	v_perm_b32 v36, v240, v141, s42
	v_perm_b32 v37, v240, v141, s43
	v_perm_b32 v42, v240, v142, s42
	v_perm_b32 v43, v240, v142, s43
	v_perm_b32 v44, v240, v143, s42
	v_perm_b32 v45, v240, v143, s43
	v_pk_add_f16 v34, v34, s5 op_sel_hi:[1,0]
	v_pk_add_f16 v35, v35, s5 op_sel_hi:[1,0]
	v_pk_add_f16 v36, v36, s5 op_sel_hi:[1,0]
	v_pk_add_f16 v37, v37, s5 op_sel_hi:[1,0]
	v_pk_add_f16 v42, v42, s5 op_sel_hi:[1,0]
	v_pk_add_f16 v43, v43, s5 op_sel_hi:[1,0]
	v_pk_add_f16 v44, v44, s5 op_sel_hi:[1,0]
	v_pk_add_f16 v45, v45, s5 op_sel_hi:[1,0]
	v_mfma_f32_32x32x16_f16 v[18:33], v[46:49], v[34:37], v[18:33]
	global_load_dwordx2 v[154:155], v241, s[0:1] offset:2560
	global_load_dwordx2 v[152:153], v241, s[0:1] offset:3072
	global_load_dwordx2 v[150:151], v241, s[0:1] offset:3584
	v_mov_b32_e32 v148, v0
	s_or_b32 s0, s8, 4
	s_ashr_i32 s1, s0, 31
	s_lshl_b64 s[0:1], s[0:1], 12
	v_mfma_f32_32x32x16_f16 v[2:17], v[46:49], v[42:45], v[2:17]
	s_nop 7
	s_nop 4
	v_cvt_pk_f16_f32 v254, v2, v3
	v_cvt_pk_f16_f32 v255, v4, v5
	ds_write_b64 v251, v[254:255] offset:0
	v_mov_b32_e32 v222, v2
	v_mov_b32_e32 v223, v3
	v_pk_mul_f32 v[194:195], v[2:3], v[2:3]
	v_mov_b32_e32 v220, v4
	v_mov_b32_e32 v221, v5
	v_pk_mul_f32 v[192:193], v[4:5], v[4:5]
	v_cvt_pk_f16_f32 v252, v6, v7
	v_cvt_pk_f16_f32 v253, v8, v9
	ds_write_b64 v251, v[252:253] offset:16
	v_mov_b32_e32 v218, v6
	v_mov_b32_e32 v219, v7
	v_pk_mul_f32 v[184:185], v[6:7], v[6:7]
	v_mov_b32_e32 v216, v8
	v_mov_b32_e32 v217, v9
	v_pk_mul_f32 v[166:167], v[8:9], v[8:9]
	v_cvt_pk_f16_f32 v254, v10, v11
	v_cvt_pk_f16_f32 v255, v12, v13
	ds_write_b64 v251, v[254:255] offset:32
	v_mov_b32_e32 v214, v10
	v_mov_b32_e32 v215, v11
	v_pk_mul_f32 v[164:165], v[10:11], v[10:11]
	v_mov_b32_e32 v204, v12
	v_mov_b32_e32 v205, v13
	v_pk_mul_f32 v[162:163], v[12:13], v[12:13]
	v_cvt_pk_f16_f32 v252, v14, v15
	v_cvt_pk_f16_f32 v253, v16, v17
	ds_write_b64 v251, v[252:253] offset:48
	v_mov_b32_e32 v202, v14
	v_mov_b32_e32 v203, v15
	v_pk_mul_f32 v[160:161], v[14:15], v[14:15]
	v_mov_b32_e32 v196, v16
	v_mov_b32_e32 v197, v17
	v_pk_mul_f32 v[156:157], v[16:17], v[16:17]
	v_cvt_pk_f16_f32 v254, v18, v19
	v_cvt_pk_f16_f32 v255, v20, v21
	ds_write_b64 v251, v[254:255] offset:4608
	v_pk_add_f32 v[222:223], v[222:223], v[18:19]
	v_pk_fma_f32 v[194:195], v[18:19], v[18:19], v[194:195]
	v_pk_add_f32 v[220:221], v[220:221], v[20:21]
	v_pk_fma_f32 v[192:193], v[20:21], v[20:21], v[192:193]
	v_cvt_pk_f16_f32 v252, v22, v23
	v_cvt_pk_f16_f32 v253, v24, v25
	ds_write_b64 v251, v[252:253] offset:4624
	v_pk_add_f32 v[218:219], v[218:219], v[22:23]
	v_pk_fma_f32 v[184:185], v[22:23], v[22:23], v[184:185]
	v_pk_add_f32 v[216:217], v[216:217], v[24:25]
	v_pk_fma_f32 v[166:167], v[24:25], v[24:25], v[166:167]
	v_cvt_pk_f16_f32 v254, v26, v27
	v_cvt_pk_f16_f32 v255, v28, v29
	ds_write_b64 v251, v[254:255] offset:4640
	v_pk_add_f32 v[214:215], v[214:215], v[26:27]
	v_pk_fma_f32 v[164:165], v[26:27], v[26:27], v[164:165]
	v_pk_add_f32 v[204:205], v[204:205], v[28:29]
	v_pk_fma_f32 v[162:163], v[28:29], v[28:29], v[162:163]
	v_cvt_pk_f16_f32 v252, v30, v31
	v_cvt_pk_f16_f32 v253, v32, v33
	ds_write_b64 v251, v[252:253] offset:4656
	v_pk_add_f32 v[202:203], v[202:203], v[30:31]
	v_pk_fma_f32 v[160:161], v[30:31], v[30:31], v[160:161]
	v_pk_add_f32 v[196:197], v[196:197], v[32:33]
	v_pk_fma_f32 v[156:157], v[32:33], v[32:33], v[156:157]
	s_nop 3
	s_nop 0
	s_waitcnt lgkmcnt(0)
	s_barrier
	s_nop 4
	ds_read_b128 v[2:5], v159 offset:34816
	ds_read_b128 v[18:21], v159 offset:43520
	ds_read_b128 v[140:143], v159 offset:34848
	ds_read_b128 v[144:147], v159 offset:43552
	s_waitcnt lgkmcnt(3)
	v_mfma_f32_32x32x16_f16 v[50:65], v[2:5], v[126:129], 0
	s_add_u32 s0, s2, s0
	s_addc_u32 s1, s3, s1
	s_waitcnt lgkmcnt(2)
	v_mfma_f32_32x32x16_f16 v[34:49], v[18:21], v[126:129], 0
	v_mfma_f32_32x32x16_f16 v[2:17], v[122:125], v[2:5], v[168:183]
	v_mfma_f32_32x32x16_f16 v[18:33], v[122:125], v[18:21], v[168:183]
	ds_read_b128 v[242:245], v159 offset:34880
	ds_read_b128 v[246:249], v159 offset:43584
	s_waitcnt lgkmcnt(3)
	v_mfma_f32_32x32x16_f16 v[50:65], v[140:143], v[118:121], v[50:65]
	s_waitcnt lgkmcnt(2)
	v_mfma_f32_32x32x16_f16 v[34:49], v[144:147], v[118:121], v[34:49]
	v_mfma_f32_32x32x16_f16 v[2:17], v[114:117], v[140:143], v[2:17]
	v_mfma_f32_32x32x16_f16 v[18:33], v[114:117], v[144:147], v[18:33]
	ds_read_b128 v[140:143], v159 offset:34912
	ds_read_b128 v[144:147], v159 offset:43616
	s_waitcnt lgkmcnt(3)
	v_mfma_f32_32x32x16_f16 v[50:65], v[242:245], v[110:113], v[50:65]
	s_waitcnt lgkmcnt(2)
	v_mfma_f32_32x32x16_f16 v[34:49], v[246:249], v[110:113], v[34:49]
	v_mfma_f32_32x32x16_f16 v[2:17], v[106:109], v[242:245], v[2:17]
	v_mfma_f32_32x32x16_f16 v[18:33], v[106:109], v[246:249], v[18:33]
	ds_read_b128 v[242:245], v159 offset:34944
	ds_read_b128 v[246:249], v159 offset:43648
	s_waitcnt lgkmcnt(3)
	v_mfma_f32_32x32x16_f16 v[50:65], v[140:143], v[102:105], v[50:65]
	s_waitcnt lgkmcnt(2)
	v_mfma_f32_32x32x16_f16 v[34:49], v[144:147], v[102:105], v[34:49]
	v_mfma_f32_32x32x16_f16 v[2:17], v[98:101], v[140:143], v[2:17]
	v_mfma_f32_32x32x16_f16 v[18:33], v[98:101], v[144:147], v[18:33]
	ds_read_b128 v[186:189], v159 offset:34976
	ds_read_b128 v[206:209], v159 offset:43680
	s_waitcnt lgkmcnt(3)
	v_mfma_f32_32x32x16_f16 v[50:65], v[242:245], v[94:97], v[50:65]
	s_waitcnt lgkmcnt(2)
	v_mfma_f32_32x32x16_f16 v[34:49], v[246:249], v[94:97], v[34:49]
	v_mfma_f32_32x32x16_f16 v[2:17], v[86:89], v[242:245], v[2:17]
	v_mfma_f32_32x32x16_f16 v[18:33], v[86:89], v[246:249], v[18:33]
	ds_read_b128 v[140:143], v159 offset:35008
	ds_read_b128 v[144:147], v159 offset:43712
	s_waitcnt lgkmcnt(3)
	v_mfma_f32_32x32x16_f16 v[50:65], v[186:189], v[90:93], v[50:65]
	s_waitcnt lgkmcnt(2)
	v_mfma_f32_32x32x16_f16 v[34:49], v[206:209], v[90:93], v[34:49]
	v_mfma_f32_32x32x16_f16 v[2:17], v[78:81], v[186:189], v[2:17]
	v_mfma_f32_32x32x16_f16 v[18:33], v[78:81], v[206:209], v[18:33]
	ds_read_b128 v[186:189], v159 offset:35040
	ds_read_b128 v[206:209], v159 offset:43744
	s_waitcnt lgkmcnt(3)
	v_mfma_f32_32x32x16_f16 v[50:65], v[140:143], v[82:85], v[50:65]
	s_waitcnt lgkmcnt(2)
	v_mfma_f32_32x32x16_f16 v[34:49], v[144:147], v[82:85], v[34:49]
	v_mfma_f32_32x32x16_f16 v[2:17], v[70:73], v[140:143], v[2:17]
	v_lshlrev_b32_e32 v140, 3, v148
	v_and_b32_e32 v199, 0x1f8, v140
	global_load_dwordx2 v[148:149], v199, s[0:1]
	global_load_dwordx2 v[142:143], v199, s[0:1] offset:1024
	global_load_dwordx2 v[140:141], v199, s[0:1] offset:1536
	v_mfma_f32_32x32x16_f16 v[18:33], v[70:73], v[144:147], v[18:33]
	global_load_dwordx2 v[144:145], v199, s[0:1] offset:512
	global_load_dwordx2 v[146:147], v199, s[0:1] offset:2048
	s_waitcnt lgkmcnt(1)
	v_mfma_f32_32x32x16_f16 v[50:65], v[186:189], v[74:77], v[50:65]
	v_mfma_f32_32x32x16_f16 v[2:17], v[66:69], v[186:189], v[2:17]
	s_nop 10
	v_cvt_pk_f16_f32 v57, v56, v57
	v_cvt_pk_f16_f32 v56, v54, v55
	v_cvt_pk_f16_f32 v54, v50, v51
	s_waitcnt vmcnt(12)
	v_cvt_pk_f16_f32 v55, v52, v53
	s_waitcnt vmcnt(8)
	v_perm_b32 v50, v240, v138, s42
	v_perm_b32 v51, v240, v138, s43
	v_perm_b32 v52, v240, v139, s42
	v_perm_b32 v53, v240, v139, s43
	v_perm_b32 v139, v240, v136, s43
	v_pk_add_f16 v50, v50, s5 op_sel_hi:[1,0]
	v_pk_add_f16 v51, v51, s5 op_sel_hi:[1,0]
	v_pk_add_f16 v52, v52, s5 op_sel_hi:[1,0]
	v_pk_add_f16 v53, v53, s5 op_sel_hi:[1,0]
	v_perm_b32 v190, v240, v137, s42
	s_waitcnt lgkmcnt(0)
	v_mfma_f32_32x32x16_f16 v[18:33], v[66:69], v[206:209], v[18:33]
	v_perm_b32 v138, v240, v136, s42
	v_perm_b32 v191, v240, v137, s43
	v_pk_add_f16 v136, v138, s5 op_sel_hi:[1,0]
	v_pk_add_f16 v137, v139, s5 op_sel_hi:[1,0]
	v_pk_add_f16 v138, v190, s5 op_sel_hi:[1,0]
	v_pk_add_f16 v139, v191, s5 op_sel_hi:[1,0]
	v_cvt_pk_f16_f32 v65, v64, v65
	v_cvt_pk_f16_f32 v64, v62, v63
	v_cvt_pk_f16_f32 v63, v60, v61
	v_cvt_pk_f16_f32 v62, v58, v59
	v_mfma_f32_32x32x16_f16 v[34:49], v[206:209], v[74:77], v[34:49]
	v_mfma_f32_32x32x16_f16 v[2:17], v[54:57], v[50:53], v[2:17]
	s_waitcnt vmcnt(7)
	v_perm_b32 v58, v240, v134, s42
	v_perm_b32 v59, v240, v134, s43
	v_perm_b32 v60, v240, v135, s42
	v_perm_b32 v61, v240, v135, s43
	v_pk_add_f16 v58, v58, s5 op_sel_hi:[1,0]
	v_pk_add_f16 v59, v59, s5 op_sel_hi:[1,0]
	v_pk_add_f16 v60, v60, s5 op_sel_hi:[1,0]
	v_pk_add_f16 v61, v61, s5 op_sel_hi:[1,0]
	v_mfma_f32_32x32x16_f16 v[18:33], v[54:57], v[136:139], v[18:33]
	v_perm_b32 v134, v240, v154, s42
	v_perm_b32 v135, v240, v154, s43
	v_perm_b32 v154, v240, v155, s42
	v_perm_b32 v155, v240, v155, s43
	v_pk_add_f16 v210, v134, s5 op_sel_hi:[1,0]
	v_pk_add_f16 v211, v135, s5 op_sel_hi:[1,0]
	v_pk_add_f16 v212, v154, s5 op_sel_hi:[1,0]
	v_pk_add_f16 v213, v155, s5 op_sel_hi:[1,0]
	v_cvt_pk_f16_f32 v41, v40, v41
	v_cvt_pk_f16_f32 v40, v38, v39
	v_cvt_pk_f16_f32 v39, v36, v37
	v_cvt_pk_f16_f32 v38, v34, v35
	v_mfma_f32_32x32x16_f16 v[2:17], v[62:65], v[58:61], v[2:17]
	v_perm_b32 v34, v240, v132, s42
	v_perm_b32 v35, v240, v132, s43
	v_perm_b32 v36, v240, v133, s42
	v_perm_b32 v37, v240, v133, s43
	v_pk_add_f16 v34, v34, s5 op_sel_hi:[1,0]
	v_pk_add_f16 v35, v35, s5 op_sel_hi:[1,0]
	v_pk_add_f16 v36, v36, s5 op_sel_hi:[1,0]
	v_pk_add_f16 v37, v37, s5 op_sel_hi:[1,0]
	s_waitcnt vmcnt(6)
	v_mfma_f32_32x32x16_f16 v[18:33], v[62:65], v[210:213], v[18:33]
	v_perm_b32 v132, v240, v152, s42
	v_perm_b32 v133, v240, v152, s43
	v_perm_b32 v134, v240, v153, s42
	v_perm_b32 v53, v240, v153, s43
	v_pk_add_f16 v50, v132, s5 op_sel_hi:[1,0]
	v_pk_add_f16 v51, v133, s5 op_sel_hi:[1,0]
	v_pk_add_f16 v52, v134, s5 op_sel_hi:[1,0]
	v_pk_add_f16 v53, v53, s5 op_sel_hi:[1,0]
	v_cvt_pk_f16_f32 v49, v48, v49
	v_cvt_pk_f16_f32 v48, v46, v47
	v_cvt_pk_f16_f32 v47, v44, v45
	v_cvt_pk_f16_f32 v46, v42, v43
	v_mfma_f32_32x32x16_f16 v[2:17], v[38:41], v[34:37], v[2:17]
	v_perm_b32 v42, v240, v130, s42
	v_perm_b32 v43, v240, v130, s43
	v_perm_b32 v44, v240, v131, s42
	v_perm_b32 v45, v240, v131, s43
	v_pk_add_f16 v42, v42, s5 op_sel_hi:[1,0]
	v_pk_add_f16 v43, v43, s5 op_sel_hi:[1,0]
	v_pk_add_f16 v44, v44, s5 op_sel_hi:[1,0]
	v_pk_add_f16 v45, v45, s5 op_sel_hi:[1,0]
	s_waitcnt vmcnt(5)
	v_mfma_f32_32x32x16_f16 v[18:33], v[38:41], v[50:53], v[18:33]
	v_perm_b32 v34, v240, v150, s42
	v_perm_b32 v35, v240, v150, s43
	v_perm_b32 v36, v240, v151, s42
	v_perm_b32 v37, v240, v151, s43
	v_pk_add_f16 v34, v34, s5 op_sel_hi:[1,0]
	v_pk_add_f16 v35, v35, s5 op_sel_hi:[1,0]
	v_pk_add_f16 v36, v36, s5 op_sel_hi:[1,0]
	v_pk_add_f16 v37, v37, s5 op_sel_hi:[1,0]
	v_mfma_f32_32x32x16_f16 v[2:17], v[46:49], v[42:45], v[2:17]
	global_load_dwordx2 v[154:155], v199, s[0:1] offset:2560
	global_load_dwordx2 v[152:153], v199, s[0:1] offset:3072
	global_load_dwordx2 v[150:151], v199, s[0:1] offset:3584
	s_or_b32 s0, s8, 6
	s_ashr_i32 s1, s0, 31
	s_lshl_b64 s[0:1], s[0:1], 12
	s_add_u32 s0, s2, s0
	v_mfma_f32_32x32x16_f16 v[18:33], v[46:49], v[34:37], v[18:33]
	s_nop 7
	s_nop 4
	v_cvt_pk_f16_f32 v254, v2, v3
	v_cvt_pk_f16_f32 v255, v4, v5
	ds_write_b64 v251, v[254:255] offset:18432
	v_pk_add_f32 v[222:223], v[222:223], v[2:3]
	v_pk_fma_f32 v[194:195], v[2:3], v[2:3], v[194:195]
	v_pk_add_f32 v[220:221], v[220:221], v[4:5]
	v_pk_fma_f32 v[192:193], v[4:5], v[4:5], v[192:193]
	v_cvt_pk_f16_f32 v252, v6, v7
	v_cvt_pk_f16_f32 v253, v8, v9
	ds_write_b64 v251, v[252:253] offset:18448
	v_pk_add_f32 v[218:219], v[218:219], v[6:7]
	v_pk_fma_f32 v[184:185], v[6:7], v[6:7], v[184:185]
	v_pk_add_f32 v[216:217], v[216:217], v[8:9]
	v_pk_fma_f32 v[166:167], v[8:9], v[8:9], v[166:167]
	v_cvt_pk_f16_f32 v254, v10, v11
	v_cvt_pk_f16_f32 v255, v12, v13
	ds_write_b64 v251, v[254:255] offset:18464
	v_pk_add_f32 v[214:215], v[214:215], v[10:11]
	v_pk_fma_f32 v[164:165], v[10:11], v[10:11], v[164:165]
	v_pk_add_f32 v[204:205], v[204:205], v[12:13]
	v_pk_fma_f32 v[162:163], v[12:13], v[12:13], v[162:163]
	v_cvt_pk_f16_f32 v252, v14, v15
	v_cvt_pk_f16_f32 v253, v16, v17
	ds_write_b64 v251, v[252:253] offset:18480
	v_pk_add_f32 v[202:203], v[202:203], v[14:15]
	v_pk_fma_f32 v[160:161], v[14:15], v[14:15], v[160:161]
	v_pk_add_f32 v[196:197], v[196:197], v[16:17]
	v_pk_fma_f32 v[156:157], v[16:17], v[16:17], v[156:157]
	v_cvt_pk_f16_f32 v254, v18, v19
	v_cvt_pk_f16_f32 v255, v20, v21
	ds_write_b64 v251, v[254:255] offset:23040
	v_pk_add_f32 v[222:223], v[222:223], v[18:19]
	v_pk_fma_f32 v[194:195], v[18:19], v[18:19], v[194:195]
	v_pk_add_f32 v[220:221], v[220:221], v[20:21]
	v_pk_fma_f32 v[192:193], v[20:21], v[20:21], v[192:193]
	v_cvt_pk_f16_f32 v252, v22, v23
	v_cvt_pk_f16_f32 v253, v24, v25
	ds_write_b64 v251, v[252:253] offset:23056
	v_pk_add_f32 v[218:219], v[218:219], v[22:23]
	v_pk_fma_f32 v[184:185], v[22:23], v[22:23], v[184:185]
	v_pk_add_f32 v[216:217], v[216:217], v[24:25]
	v_pk_fma_f32 v[166:167], v[24:25], v[24:25], v[166:167]
	v_cvt_pk_f16_f32 v254, v26, v27
	v_cvt_pk_f16_f32 v255, v28, v29
	ds_write_b64 v251, v[254:255] offset:23072
	v_pk_add_f32 v[214:215], v[214:215], v[26:27]
	v_pk_fma_f32 v[164:165], v[26:27], v[26:27], v[164:165]
	v_pk_add_f32 v[204:205], v[204:205], v[28:29]
	v_pk_fma_f32 v[162:163], v[28:29], v[28:29], v[162:163]
	v_cvt_pk_f16_f32 v252, v30, v31
	v_cvt_pk_f16_f32 v253, v32, v33
	ds_write_b64 v251, v[252:253] offset:23088
	v_pk_add_f32 v[202:203], v[202:203], v[30:31]
	v_pk_fma_f32 v[160:161], v[30:31], v[30:31], v[160:161]
	v_pk_add_f32 v[196:197], v[196:197], v[32:33]
	v_pk_fma_f32 v[156:157], v[32:33], v[32:33], v[156:157]
	s_nop 3
	s_nop 0
	s_nop 0
	s_waitcnt lgkmcnt(0)
	s_barrier
	ds_read_b128 v[2:5], v159
	s_nop 2
	ds_read_b128 v[18:21], v159 offset:8704
	s_waitcnt lgkmcnt(1)
	v_mfma_f32_32x32x16_f16 v[50:65], v[2:5], v[126:129], 0
	v_lshlrev_b32_e32 v0, 3, v0
	s_addc_u32 s1, s3, s1
	v_and_b32_e32 v0, 0x1f8, v0
	global_load_dwordx2 v[138:139], v0, s[0:1]
	s_waitcnt lgkmcnt(0)
	v_mfma_f32_32x32x16_f16 v[34:49], v[18:21], v[126:129], 0
	v_mfma_f32_32x32x16_f16 v[2:17], v[122:125], v[2:5], v[168:183]
	v_mfma_f32_32x32x16_f16 v[18:33], v[122:125], v[18:21], v[168:183]
	ds_read_b128 v[130:133], v159 offset:32
	ds_read_b128 v[134:137], v159 offset:8736
	s_waitcnt lgkmcnt(1)
	v_mfma_f32_32x32x16_f16 v[50:65], v[130:133], v[118:121], v[50:65]
	s_waitcnt lgkmcnt(0)
	v_mfma_f32_32x32x16_f16 v[34:49], v[134:137], v[118:121], v[34:49]
	v_mfma_f32_32x32x16_f16 v[2:17], v[114:117], v[130:133], v[2:17]
	v_mfma_f32_32x32x16_f16 v[18:33], v[114:117], v[134:137], v[18:33]
	ds_read_b128 v[224:227], v159 offset:64
	ds_read_b128 v[228:231], v159 offset:8768
	ds_read_b128 v[130:133], v159 offset:96
	ds_read_b128 v[134:137], v159 offset:8800
	s_waitcnt lgkmcnt(3)
	v_mfma_f32_32x32x16_f16 v[50:65], v[224:227], v[110:113], v[50:65]
	s_waitcnt lgkmcnt(2)
	v_mfma_f32_32x32x16_f16 v[34:49], v[228:231], v[110:113], v[34:49]
	v_mfma_f32_32x32x16_f16 v[2:17], v[106:109], v[224:227], v[2:17]
	v_mfma_f32_32x32x16_f16 v[18:33], v[106:109], v[228:231], v[18:33]
	ds_read_b128 v[224:227], v159 offset:128
	ds_read_b128 v[228:231], v159 offset:8832
	s_waitcnt lgkmcnt(3)
	v_mfma_f32_32x32x16_f16 v[50:65], v[130:133], v[102:105], v[50:65]
	s_waitcnt lgkmcnt(2)
	v_mfma_f32_32x32x16_f16 v[34:49], v[134:137], v[102:105], v[34:49]
	v_mfma_f32_32x32x16_f16 v[2:17], v[98:101], v[130:133], v[2:17]
	v_mfma_f32_32x32x16_f16 v[18:33], v[98:101], v[134:137], v[18:33]
	ds_read_b128 v[130:133], v159 offset:160
	ds_read_b128 v[134:137], v159 offset:8864
	s_waitcnt lgkmcnt(3)
	v_mfma_f32_32x32x16_f16 v[50:65], v[224:227], v[94:97], v[50:65]
	s_waitcnt lgkmcnt(2)
	v_mfma_f32_32x32x16_f16 v[34:49], v[228:231], v[94:97], v[34:49]
	v_mfma_f32_32x32x16_f16 v[2:17], v[86:89], v[224:227], v[2:17]
	v_mfma_f32_32x32x16_f16 v[18:33], v[86:89], v[228:231], v[18:33]
	ds_read_b128 v[224:227], v159 offset:192
	ds_read_b128 v[228:231], v159 offset:8896
	s_waitcnt lgkmcnt(3)
	v_mfma_f32_32x32x16_f16 v[50:65], v[130:133], v[90:93], v[50:65]
	s_waitcnt lgkmcnt(2)
	v_mfma_f32_32x32x16_f16 v[34:49], v[134:137], v[90:93], v[34:49]
	v_mfma_f32_32x32x16_f16 v[2:17], v[78:81], v[130:133], v[2:17]
	v_mfma_f32_32x32x16_f16 v[18:33], v[78:81], v[134:137], v[18:33]
	ds_read_b128 v[232:235], v159 offset:224
	ds_read_b128 v[236:239], v159 offset:8928
	s_waitcnt lgkmcnt(3)
	v_mfma_f32_32x32x16_f16 v[50:65], v[224:227], v[82:85], v[50:65]
	global_load_dwordx2 v[134:135], v0, s[0:1] offset:512
	global_load_dwordx2 v[132:133], v0, s[0:1] offset:1024
	global_load_dwordx2 v[130:131], v0, s[0:1] offset:1536
	s_waitcnt lgkmcnt(2)
	v_mfma_f32_32x32x16_f16 v[34:49], v[228:231], v[82:85], v[34:49]
	global_load_dwordx2 v[136:137], v0, s[0:1] offset:2048
	v_mfma_f32_32x32x16_f16 v[2:17], v[70:73], v[224:227], v[2:17]
	v_mfma_f32_32x32x16_f16 v[18:33], v[70:73], v[228:231], v[18:33]
	s_waitcnt lgkmcnt(1)
	v_mfma_f32_32x32x16_f16 v[50:65], v[232:235], v[74:77], v[50:65]
	v_mfma_f32_32x32x16_f16 v[2:17], v[66:69], v[232:235], v[2:17]
	s_nop 10
	v_cvt_pk_f16_f32 v57, v56, v57
	v_cvt_pk_f16_f32 v56, v54, v55
	v_cvt_pk_f16_f32 v54, v50, v51
	s_waitcnt vmcnt(12)
	v_lshlrev_b32_e32 v50, 8, v148
	v_cvt_pk_f16_f32 v55, v52, v53
	v_perm_b32 v50, v50, v148, s4
	v_lshrrev_b32_e32 v51, 16, v148
	v_lshrrev_b32_e32 v52, 8, v148
	v_lshrrev_b32_e32 v53, 16, v149
	v_lshrrev_b32_e32 v148, 8, v149
	v_perm_b32 v51, v52, v51, s4
	v_lshlrev_b32_e32 v52, 8, v149
	v_perm_b32 v53, v148, v53, s4
	s_waitcnt vmcnt(8)
	v_perm_b32 v52, v52, v149, s4
	v_perm_b32 v149, v240, v146, s43
	v_perm_b32 v198, v240, v147, s42
	s_waitcnt lgkmcnt(0)
	v_mfma_f32_32x32x16_f16 v[18:33], v[66:69], v[236:239], v[18:33]
	v_or_b32_e32 v50, 0x64006400, v50
	v_or_b32_e32 v51, 0x64006400, v51
	v_or_b32_e32 v52, 0x64006400, v52
	v_or_b32_e32 v53, 0x64006400, v53
	v_pk_add_f16 v50, v50, s5 op_sel_hi:[1,0]
	v_pk_add_f16 v51, v51, s5 op_sel_hi:[1,0]
	v_pk_add_f16 v52, v52, s5 op_sel_hi:[1,0]
	v_pk_add_f16 v53, v53, s5 op_sel_hi:[1,0]
	v_perm_b32 v148, v240, v146, s42
	v_perm_b32 v200, v240, v147, s43
	v_pk_add_f16 v146, v148, s5 op_sel_hi:[1,0]
	v_pk_add_f16 v147, v149, s5 op_sel_hi:[1,0]
	v_pk_add_f16 v148, v198, s5 op_sel_hi:[1,0]
	v_pk_add_f16 v149, v200, s5 op_sel_hi:[1,0]
	v_cvt_pk_f16_f32 v65, v64, v65
	v_cvt_pk_f16_f32 v64, v62, v63
	v_cvt_pk_f16_f32 v62, v58, v59
	v_cvt_pk_f16_f32 v63, v60, v61
	s_waitcnt vmcnt(7)
	v_mfma_f32_32x32x16_f16 v[34:49], v[236:239], v[74:77], v[34:49]
	v_mfma_f32_32x32x16_f16 v[2:17], v[54:57], v[50:53], v[2:17]
	v_perm_b32 v58, v240, v144, s42
	v_perm_b32 v59, v240, v144, s43
	v_perm_b32 v60, v240, v145, s42
	v_perm_b32 v61, v240, v145, s43
	v_mfma_f32_32x32x16_f16 v[18:33], v[54:57], v[146:149], v[18:33]
	v_pk_add_f16 v58, v58, s5 op_sel_hi:[1,0]
	v_pk_add_f16 v59, v59, s5 op_sel_hi:[1,0]
	v_pk_add_f16 v60, v60, s5 op_sel_hi:[1,0]
	v_pk_add_f16 v61, v61, s5 op_sel_hi:[1,0]
	v_perm_b32 v144, v240, v154, s42
	v_perm_b32 v145, v240, v154, s43
	v_perm_b32 v154, v240, v155, s42
	v_perm_b32 v155, v240, v155, s43
	v_pk_add_f16 v224, v144, s5 op_sel_hi:[1,0]
	v_pk_add_f16 v225, v145, s5 op_sel_hi:[1,0]
	v_pk_add_f16 v226, v154, s5 op_sel_hi:[1,0]
	v_pk_add_f16 v227, v155, s5 op_sel_hi:[1,0]
	v_cvt_pk_f16_f32 v41, v40, v41
	v_cvt_pk_f16_f32 v40, v38, v39
	v_cvt_pk_f16_f32 v39, v36, v37
	v_cvt_pk_f16_f32 v38, v34, v35
	s_waitcnt vmcnt(6)
	v_mfma_f32_32x32x16_f16 v[2:17], v[62:65], v[58:61], v[2:17]
	v_perm_b32 v34, v240, v142, s42
	v_perm_b32 v35, v240, v142, s43
	v_mfma_f32_32x32x16_f16 v[18:33], v[62:65], v[224:227], v[18:33]
	v_perm_b32 v36, v240, v143, s42
	v_perm_b32 v37, v240, v143, s43
	v_pk_add_f16 v34, v34, s5 op_sel_hi:[1,0]
	v_pk_add_f16 v35, v35, s5 op_sel_hi:[1,0]
	v_pk_add_f16 v36, v36, s5 op_sel_hi:[1,0]
	v_pk_add_f16 v37, v37, s5 op_sel_hi:[1,0]
	v_perm_b32 v142, v240, v152, s42
	v_perm_b32 v143, v240, v152, s43
	v_perm_b32 v144, v240, v153, s42
	v_perm_b32 v53, v240, v153, s43
	v_pk_add_f16 v50, v142, s5 op_sel_hi:[1,0]
	v_pk_add_f16 v51, v143, s5 op_sel_hi:[1,0]
	v_pk_add_f16 v52, v144, s5 op_sel_hi:[1,0]
	v_pk_add_f16 v53, v53, s5 op_sel_hi:[1,0]
	v_cvt_pk_f16_f32 v49, v48, v49
	v_cvt_pk_f16_f32 v48, v46, v47
	v_cvt_pk_f16_f32 v47, v44, v45
	v_cvt_pk_f16_f32 v46, v42, v43
	v_mfma_f32_32x32x16_f16 v[2:17], v[38:41], v[34:37], v[2:17]
	s_waitcnt vmcnt(5)
	v_mfma_f32_32x32x16_f16 v[18:33], v[38:41], v[50:53], v[18:33]
	v_perm_b32 v42, v240, v140, s42
	v_perm_b32 v43, v240, v140, s43
	v_perm_b32 v44, v240, v141, s42
	v_perm_b32 v45, v240, v141, s43
	v_perm_b32 v34, v240, v150, s42
	v_perm_b32 v35, v240, v150, s43
	v_perm_b32 v36, v240, v151, s42
	v_perm_b32 v37, v240, v151, s43
	v_pk_add_f16 v42, v42, s5 op_sel_hi:[1,0]
	v_pk_add_f16 v43, v43, s5 op_sel_hi:[1,0]
	v_pk_add_f16 v44, v44, s5 op_sel_hi:[1,0]
	v_pk_add_f16 v45, v45, s5 op_sel_hi:[1,0]
	v_pk_add_f16 v34, v34, s5 op_sel_hi:[1,0]
	v_pk_add_f16 v35, v35, s5 op_sel_hi:[1,0]
	v_pk_add_f16 v36, v36, s5 op_sel_hi:[1,0]
	v_pk_add_f16 v37, v37, s5 op_sel_hi:[1,0]
	v_mfma_f32_32x32x16_f16 v[2:17], v[46:49], v[42:45], v[2:17]
	global_load_dwordx2 v[142:143], v0, s[0:1] offset:2560
	global_load_dwordx2 v[140:141], v0, s[0:1] offset:3072
	global_load_dwordx2 v[64:65], v0, s[0:1] offset:3584
	v_mfma_f32_32x32x16_f16 v[18:33], v[46:49], v[34:37], v[18:33]
	s_nop 7
	s_nop 4
	v_cvt_pk_f16_f32 v254, v2, v3
	v_cvt_pk_f16_f32 v255, v4, v5
	ds_write_b64 v251, v[254:255] offset:0
	v_pk_add_f32 v[222:223], v[222:223], v[2:3]
	v_pk_fma_f32 v[194:195], v[2:3], v[2:3], v[194:195]
	v_pk_add_f32 v[220:221], v[220:221], v[4:5]
	v_pk_fma_f32 v[192:193], v[4:5], v[4:5], v[192:193]
	v_cvt_pk_f16_f32 v252, v6, v7
	v_cvt_pk_f16_f32 v253, v8, v9
	ds_write_b64 v251, v[252:253] offset:16
	v_pk_add_f32 v[218:219], v[218:219], v[6:7]
	v_pk_fma_f32 v[184:185], v[6:7], v[6:7], v[184:185]
	v_pk_add_f32 v[216:217], v[216:217], v[8:9]
	v_pk_fma_f32 v[166:167], v[8:9], v[8:9], v[166:167]
	v_cvt_pk_f16_f32 v254, v10, v11
	v_cvt_pk_f16_f32 v255, v12, v13
	ds_write_b64 v251, v[254:255] offset:32
	v_pk_add_f32 v[214:215], v[214:215], v[10:11]
	v_pk_fma_f32 v[164:165], v[10:11], v[10:11], v[164:165]
	v_pk_add_f32 v[204:205], v[204:205], v[12:13]
	v_pk_fma_f32 v[162:163], v[12:13], v[12:13], v[162:163]
	v_cvt_pk_f16_f32 v252, v14, v15
	v_cvt_pk_f16_f32 v253, v16, v17
	ds_write_b64 v251, v[252:253] offset:48
	v_pk_add_f32 v[202:203], v[202:203], v[14:15]
	v_pk_fma_f32 v[160:161], v[14:15], v[14:15], v[160:161]
	v_pk_add_f32 v[196:197], v[196:197], v[16:17]
	v_pk_fma_f32 v[156:157], v[16:17], v[16:17], v[156:157]
	v_cvt_pk_f16_f32 v254, v18, v19
	v_cvt_pk_f16_f32 v255, v20, v21
	ds_write_b64 v251, v[254:255] offset:4608
	v_pk_add_f32 v[222:223], v[222:223], v[18:19]
	v_pk_fma_f32 v[194:195], v[18:19], v[18:19], v[194:195]
	v_pk_add_f32 v[220:221], v[220:221], v[20:21]
	v_pk_fma_f32 v[192:193], v[20:21], v[20:21], v[192:193]
	v_cvt_pk_f16_f32 v252, v22, v23
	v_cvt_pk_f16_f32 v253, v24, v25
	ds_write_b64 v251, v[252:253] offset:4624
	v_pk_add_f32 v[218:219], v[218:219], v[22:23]
	v_pk_fma_f32 v[184:185], v[22:23], v[22:23], v[184:185]
	v_pk_add_f32 v[216:217], v[216:217], v[24:25]
	v_pk_fma_f32 v[166:167], v[24:25], v[24:25], v[166:167]
	v_cvt_pk_f16_f32 v254, v26, v27
	v_cvt_pk_f16_f32 v255, v28, v29
	ds_write_b64 v251, v[254:255] offset:4640
	v_pk_add_f32 v[214:215], v[214:215], v[26:27]
	v_pk_fma_f32 v[164:165], v[26:27], v[26:27], v[164:165]
	v_pk_add_f32 v[204:205], v[204:205], v[28:29]
	v_pk_fma_f32 v[162:163], v[28:29], v[28:29], v[162:163]
	v_cvt_pk_f16_f32 v252, v30, v31
	v_cvt_pk_f16_f32 v253, v32, v33
	ds_write_b64 v251, v[252:253] offset:4656
	v_pk_add_f32 v[202:203], v[202:203], v[30:31]
	v_pk_fma_f32 v[160:161], v[30:31], v[30:31], v[160:161]
	v_pk_add_f32 v[196:197], v[196:197], v[32:33]
	v_pk_fma_f32 v[156:157], v[32:33], v[32:33], v[156:157]
	s_nop 7
	s_waitcnt lgkmcnt(0)
	s_barrier
	s_nop 1
	ds_read_b128 v[16:19], v159 offset:43520
	s_waitcnt lgkmcnt(0)
	v_mfma_f32_32x32x16_f16 v[32:47], v[16:19], v[126:129], 0
	ds_read_b128 v[2:5], v159 offset:34816
	s_waitcnt lgkmcnt(0)
	v_mfma_f32_32x32x16_f16 v[48:63], v[2:5], v[126:129], 0
	ds_read_b128 v[126:129], v159 offset:34848
	s_waitcnt lgkmcnt(0)
	v_mfma_f32_32x32x16_f16 v[48:63], v[126:129], v[118:121], v[48:63]
	v_mfma_f32_32x32x16_f16 v[0:15], v[122:125], v[2:5], v[168:183]
	v_mfma_f32_32x32x16_f16 v[0:15], v[114:117], v[126:129], v[0:15]
	v_mfma_f32_32x32x16_f16 v[16:31], v[122:125], v[16:19], v[168:183]
	ds_read_b128 v[122:125], v159 offset:43552
	s_waitcnt lgkmcnt(0)
	v_mfma_f32_32x32x16_f16 v[32:47], v[122:125], v[118:121], v[32:47]
	v_mfma_f32_32x32x16_f16 v[16:31], v[114:117], v[122:125], v[16:31]
	ds_read_b128 v[118:121], v159 offset:34880
	ds_read_b128 v[114:117], v159 offset:43584
	s_waitcnt lgkmcnt(1)
	v_mfma_f32_32x32x16_f16 v[48:63], v[118:121], v[110:113], v[48:63]
	s_waitcnt lgkmcnt(0)
	v_mfma_f32_32x32x16_f16 v[32:47], v[114:117], v[110:113], v[32:47]
	v_mfma_f32_32x32x16_f16 v[0:15], v[106:109], v[118:121], v[0:15]
	ds_read_b128 v[110:113], v159 offset:34912
	v_mfma_f32_32x32x16_f16 v[16:31], v[106:109], v[114:117], v[16:31]
	ds_read_b128 v[106:109], v159 offset:43616
	s_waitcnt lgkmcnt(1)
	v_mfma_f32_32x32x16_f16 v[48:63], v[110:113], v[102:105], v[48:63]
	s_waitcnt lgkmcnt(0)
	v_mfma_f32_32x32x16_f16 v[32:47], v[106:109], v[102:105], v[32:47]
	v_mfma_f32_32x32x16_f16 v[0:15], v[98:101], v[110:113], v[0:15]
	ds_read_b128 v[102:105], v159 offset:34944
	v_mfma_f32_32x32x16_f16 v[16:31], v[98:101], v[106:109], v[16:31]
	ds_read_b128 v[98:101], v159 offset:43648
	s_waitcnt lgkmcnt(1)
	v_mfma_f32_32x32x16_f16 v[48:63], v[102:105], v[94:97], v[48:63]
	s_waitcnt lgkmcnt(0)
	v_mfma_f32_32x32x16_f16 v[32:47], v[98:101], v[94:97], v[32:47]
	v_mfma_f32_32x32x16_f16 v[0:15], v[86:89], v[102:105], v[0:15]
	ds_read_b128 v[94:97], v159 offset:34976
	v_mfma_f32_32x32x16_f16 v[16:31], v[86:89], v[98:101], v[16:31]
	ds_read_b128 v[86:89], v159 offset:43680
	s_waitcnt lgkmcnt(1)
	v_mfma_f32_32x32x16_f16 v[48:63], v[94:97], v[90:93], v[48:63]
	s_waitcnt lgkmcnt(0)
	v_mfma_f32_32x32x16_f16 v[32:47], v[86:89], v[90:93], v[32:47]
	v_mfma_f32_32x32x16_f16 v[0:15], v[78:81], v[94:97], v[0:15]
	ds_read_b128 v[90:93], v159 offset:35008
	v_mfma_f32_32x32x16_f16 v[16:31], v[78:81], v[86:89], v[16:31]
	ds_read_b128 v[78:81], v159 offset:43712
	s_waitcnt lgkmcnt(1)
	v_mfma_f32_32x32x16_f16 v[48:63], v[90:93], v[82:85], v[48:63]
	s_waitcnt lgkmcnt(0)
	v_mfma_f32_32x32x16_f16 v[32:47], v[78:81], v[82:85], v[32:47]
	v_mfma_f32_32x32x16_f16 v[0:15], v[70:73], v[90:93], v[0:15]
	ds_read_b128 v[82:85], v159 offset:35040
	v_mfma_f32_32x32x16_f16 v[16:31], v[70:73], v[78:81], v[16:31]
	ds_read_b128 v[70:73], v159 offset:43744
	s_waitcnt lgkmcnt(1)
	v_mfma_f32_32x32x16_f16 v[48:63], v[82:85], v[74:77], v[48:63]
	v_mfma_f32_32x32x16_f16 v[0:15], v[66:69], v[82:85], v[0:15]
	s_nop 3
	s_nop 6
	v_cvt_pk_f16_f32 v55, v54, v55
	v_cvt_pk_f16_f32 v54, v52, v53
	v_cvt_pk_f16_f32 v53, v50, v51
	v_cvt_pk_f16_f32 v52, v48, v49
	s_waitcnt vmcnt(3)
	s_waitcnt lgkmcnt(0)
	v_mfma_f32_32x32x16_f16 v[16:31], v[66:69], v[70:73], v[16:31]
	v_lshrrev_b32_e32 v69, 16, v139
	v_mfma_f32_32x32x16_f16 v[32:47], v[70:73], v[74:77], v[32:47]
	v_lshrrev_b32_e32 v70, 8, v139
	v_perm_b32 v69, v70, v69, s4
	v_perm_b32 v66, v240, v138, s42
	v_perm_b32 v67, v240, v138, s43
	v_perm_b32 v68, v240, v139, s42
	v_or_b32_e32 v69, 0x64006400, v69
	v_pk_add_f16 v66, v66, s5 op_sel_hi:[1,0]
	v_pk_add_f16 v67, v67, s5 op_sel_hi:[1,0]
	v_pk_add_f16 v68, v68, s5 op_sel_hi:[1,0]
	v_pk_add_f16 v69, v69, s5 op_sel_hi:[1,0]
	s_nop 1
	v_mfma_f32_32x32x16_f16 v[0:15], v[52:55], v[66:69], v[0:15]
	v_perm_b32 v48, v240, v136, s42
	v_perm_b32 v49, v240, v136, s43
	v_perm_b32 v50, v240, v137, s42
	v_perm_b32 v51, v240, v137, s43
	v_pk_add_f16 v48, v48, s5 op_sel_hi:[1,0]
	v_pk_add_f16 v49, v49, s5 op_sel_hi:[1,0]
	v_pk_add_f16 v50, v50, s5 op_sel_hi:[1,0]
	v_pk_add_f16 v51, v51, s5 op_sel_hi:[1,0]
	v_cvt_pk_f16_f32 v39, v38, v39
	v_cvt_pk_f16_f32 v38, v36, v37
	v_mfma_f32_32x32x16_f16 v[16:31], v[52:55], v[48:51], v[16:31]
	v_perm_b32 v48, v240, v134, s42
	v_perm_b32 v49, v240, v134, s43
	v_perm_b32 v50, v240, v135, s42
	v_perm_b32 v51, v240, v135, s43
	v_pk_add_f16 v48, v48, s5 op_sel_hi:[1,0]
	v_pk_add_f16 v49, v49, s5 op_sel_hi:[1,0]
	v_pk_add_f16 v50, v50, s5 op_sel_hi:[1,0]
	v_pk_add_f16 v51, v51, s5 op_sel_hi:[1,0]
	v_cvt_pk_f16_f32 v55, v62, v63
	v_cvt_pk_f16_f32 v54, v60, v61
	v_cvt_pk_f16_f32 v53, v58, v59
	v_cvt_pk_f16_f32 v52, v56, v57
	s_waitcnt vmcnt(2)
	v_cvt_pk_f16_f32 v37, v34, v35
	v_mfma_f32_32x32x16_f16 v[0:15], v[52:55], v[48:51], v[0:15]
	v_perm_b32 v48, v240, v142, s42
	v_perm_b32 v49, v240, v142, s43
	v_perm_b32 v50, v240, v143, s42
	v_perm_b32 v51, v240, v143, s43
	v_pk_add_f16 v48, v48, s5 op_sel_hi:[1,0]
	v_pk_add_f16 v49, v49, s5 op_sel_hi:[1,0]
	v_pk_add_f16 v50, v50, s5 op_sel_hi:[1,0]
	v_pk_add_f16 v51, v51, s5 op_sel_hi:[1,0]
	v_cvt_pk_f16_f32 v36, v32, v33
	s_waitcnt vmcnt(1)
	v_mfma_f32_32x32x16_f16 v[16:31], v[52:55], v[48:51], v[16:31]
	v_lshrrev_b32_e32 v51, 16, v133
	v_lshrrev_b32_e32 v52, 8, v133
	v_perm_b32 v51, v52, v51, s4
	v_perm_b32 v48, v240, v132, s42
	v_perm_b32 v49, v240, v132, s43
	v_perm_b32 v50, v240, v133, s42
	v_or_b32_e32 v51, 0x64006400, v51
	v_pk_add_f16 v48, v48, s5 op_sel_hi:[1,0]
	v_pk_add_f16 v49, v49, s5 op_sel_hi:[1,0]
	v_pk_add_f16 v50, v50, s5 op_sel_hi:[1,0]
	v_pk_add_f16 v51, v51, s5 op_sel_hi:[1,0]
	s_nop 1
	v_mfma_f32_32x32x16_f16 v[0:15], v[36:39], v[48:51], v[0:15]
	v_perm_b32 v32, v240, v140, s42
	v_perm_b32 v33, v240, v140, s43
	v_perm_b32 v34, v240, v141, s42
	v_perm_b32 v35, v240, v141, s43
	v_pk_add_f16 v32, v32, s5 op_sel_hi:[1,0]
	v_pk_add_f16 v33, v33, s5 op_sel_hi:[1,0]
	v_pk_add_f16 v34, v34, s5 op_sel_hi:[1,0]
	v_pk_add_f16 v35, v35, s5 op_sel_hi:[1,0]
	s_nop 1
	v_mfma_f32_32x32x16_f16 v[16:31], v[36:39], v[32:35], v[16:31]
	v_perm_b32 v32, v240, v130, s42
	v_perm_b32 v33, v240, v130, s43
	v_perm_b32 v34, v240, v131, s42
	v_perm_b32 v35, v240, v131, s43
	v_pk_add_f16 v32, v32, s5 op_sel_hi:[1,0]
	v_pk_add_f16 v33, v33, s5 op_sel_hi:[1,0]
	v_pk_add_f16 v34, v34, s5 op_sel_hi:[1,0]
	v_pk_add_f16 v35, v35, s5 op_sel_hi:[1,0]
	v_cvt_pk_f16_f32 v39, v46, v47
	v_cvt_pk_f16_f32 v38, v44, v45
	v_cvt_pk_f16_f32 v37, v42, v43
	v_cvt_pk_f16_f32 v36, v40, v41
	s_waitcnt vmcnt(0)
	s_nop 0
	v_mfma_f32_32x32x16_f16 v[0:15], v[36:39], v[32:35], v[0:15]
	v_perm_b32 v32, v240, v64, s42
	v_perm_b32 v33, v240, v64, s43
	v_perm_b32 v34, v240, v65, s42
	v_perm_b32 v35, v240, v65, s43
	v_pk_add_f16 v32, v32, s5 op_sel_hi:[1,0]
	v_pk_add_f16 v33, v33, s5 op_sel_hi:[1,0]
	v_pk_add_f16 v34, v34, s5 op_sel_hi:[1,0]
	v_pk_add_f16 v35, v35, s5 op_sel_hi:[1,0]
	s_nop 3
	v_mfma_f32_32x32x16_f16 v[16:31], v[36:39], v[32:35], v[16:31]
	s_nop 7
	s_nop 4
	v_cvt_pk_f16_f32 v254, v0, v1
	v_cvt_pk_f16_f32 v255, v2, v3
	ds_write_b64 v251, v[254:255] offset:18432
	v_pk_add_f32 v[222:223], v[222:223], v[0:1]
	v_pk_fma_f32 v[194:195], v[0:1], v[0:1], v[194:195]
	v_pk_add_f32 v[220:221], v[220:221], v[2:3]
	v_pk_fma_f32 v[192:193], v[2:3], v[2:3], v[192:193]
	v_cvt_pk_f16_f32 v252, v4, v5
	v_cvt_pk_f16_f32 v253, v6, v7
	ds_write_b64 v251, v[252:253] offset:18448
	v_pk_add_f32 v[218:219], v[218:219], v[4:5]
	v_pk_fma_f32 v[184:185], v[4:5], v[4:5], v[184:185]
	v_pk_add_f32 v[216:217], v[216:217], v[6:7]
	v_pk_fma_f32 v[166:167], v[6:7], v[6:7], v[166:167]
	v_cvt_pk_f16_f32 v254, v8, v9
	v_cvt_pk_f16_f32 v255, v10, v11
	ds_write_b64 v251, v[254:255] offset:18464
	v_pk_add_f32 v[214:215], v[214:215], v[8:9]
	v_pk_fma_f32 v[164:165], v[8:9], v[8:9], v[164:165]
	v_pk_add_f32 v[204:205], v[204:205], v[10:11]
	v_pk_fma_f32 v[162:163], v[10:11], v[10:11], v[162:163]
	v_cvt_pk_f16_f32 v252, v12, v13
	v_cvt_pk_f16_f32 v253, v14, v15
	ds_write_b64 v251, v[252:253] offset:18480
	v_pk_add_f32 v[202:203], v[202:203], v[12:13]
	v_pk_fma_f32 v[160:161], v[12:13], v[12:13], v[160:161]
	v_pk_add_f32 v[196:197], v[196:197], v[14:15]
	v_pk_fma_f32 v[156:157], v[14:15], v[14:15], v[156:157]
	v_cvt_pk_f16_f32 v254, v16, v17
	v_cvt_pk_f16_f32 v255, v18, v19
	ds_write_b64 v251, v[254:255] offset:23040
	v_pk_add_f32 v[222:223], v[222:223], v[16:17]
	v_pk_fma_f32 v[194:195], v[16:17], v[16:17], v[194:195]
	v_pk_add_f32 v[220:221], v[220:221], v[18:19]
	v_pk_fma_f32 v[192:193], v[18:19], v[18:19], v[192:193]
	v_cvt_pk_f16_f32 v252, v20, v21
	v_cvt_pk_f16_f32 v253, v22, v23
	ds_write_b64 v251, v[252:253] offset:23056
	v_pk_add_f32 v[218:219], v[218:219], v[20:21]
	v_pk_fma_f32 v[184:185], v[20:21], v[20:21], v[184:185]
	v_pk_add_f32 v[216:217], v[216:217], v[22:23]
	v_pk_fma_f32 v[166:167], v[22:23], v[22:23], v[166:167]
	v_cvt_pk_f16_f32 v254, v24, v25
	v_cvt_pk_f16_f32 v255, v26, v27
	ds_write_b64 v251, v[254:255] offset:23072
	v_pk_add_f32 v[214:215], v[214:215], v[24:25]
	v_pk_fma_f32 v[164:165], v[24:25], v[24:25], v[164:165]
	v_pk_add_f32 v[204:205], v[204:205], v[26:27]
	v_pk_fma_f32 v[162:163], v[26:27], v[26:27], v[162:163]
	v_cvt_pk_f16_f32 v252, v28, v29
	v_cvt_pk_f16_f32 v253, v30, v31
	ds_write_b64 v251, v[252:253] offset:23088
	v_pk_add_f32 v[202:203], v[202:203], v[28:29]
	v_pk_fma_f32 v[160:161], v[28:29], v[28:29], v[160:161]
	v_pk_add_f32 v[196:197], v[196:197], v[30:31]
	v_pk_fma_f32 v[156:157], v[30:31], v[30:31], v[156:157]
	s_nop 4
	s_nop 0
	v_add_f32_dpp v222, v222, v222 row_half_mirror row_mask:0xf bank_mask:0x5
	v_add_f32_dpp v222, v223, v223 row_half_mirror row_mask:0xf bank_mask:0xa
	v_add_f32_dpp v220, v220, v220 row_half_mirror row_mask:0xf bank_mask:0x5
	v_add_f32_dpp v220, v221, v221 row_half_mirror row_mask:0xf bank_mask:0xa
	v_add_f32_dpp v218, v218, v218 row_half_mirror row_mask:0xf bank_mask:0x5
	v_add_f32_dpp v218, v219, v219 row_half_mirror row_mask:0xf bank_mask:0xa
	v_add_f32_dpp v216, v216, v216 row_half_mirror row_mask:0xf bank_mask:0x5
	v_add_f32_dpp v216, v217, v217 row_half_mirror row_mask:0xf bank_mask:0xa
	v_add_f32_dpp v214, v214, v214 row_half_mirror row_mask:0xf bank_mask:0x5
	v_add_f32_dpp v214, v215, v215 row_half_mirror row_mask:0xf bank_mask:0xa
	v_add_f32_dpp v204, v204, v204 row_half_mirror row_mask:0xf bank_mask:0x5
	v_add_f32_dpp v204, v205, v205 row_half_mirror row_mask:0xf bank_mask:0xa
	v_add_f32_dpp v202, v202, v202 row_half_mirror row_mask:0xf bank_mask:0x5
	v_add_f32_dpp v202, v203, v203 row_half_mirror row_mask:0xf bank_mask:0xa
	v_add_f32_dpp v196, v196, v196 row_half_mirror row_mask:0xf bank_mask:0x5
	v_add_f32_dpp v196, v197, v197 row_half_mirror row_mask:0xf bank_mask:0xa
	v_add_f32_dpp v194, v194, v194 row_half_mirror row_mask:0xf bank_mask:0x5
	v_add_f32_dpp v194, v195, v195 row_half_mirror row_mask:0xf bank_mask:0xa
	v_add_f32_dpp v192, v192, v192 row_half_mirror row_mask:0xf bank_mask:0x5
	v_add_f32_dpp v192, v193, v193 row_half_mirror row_mask:0xf bank_mask:0xa
	v_add_f32_dpp v184, v184, v184 row_half_mirror row_mask:0xf bank_mask:0x5
	v_add_f32_dpp v184, v185, v185 row_half_mirror row_mask:0xf bank_mask:0xa
	v_add_f32_dpp v166, v166, v166 row_half_mirror row_mask:0xf bank_mask:0x5
	v_add_f32_dpp v166, v167, v167 row_half_mirror row_mask:0xf bank_mask:0xa
	v_add_f32_dpp v164, v164, v164 row_half_mirror row_mask:0xf bank_mask:0x5
	v_add_f32_dpp v164, v165, v165 row_half_mirror row_mask:0xf bank_mask:0xa
	v_add_f32_dpp v162, v162, v162 row_half_mirror row_mask:0xf bank_mask:0x5
	v_add_f32_dpp v162, v163, v163 row_half_mirror row_mask:0xf bank_mask:0xa
	v_add_f32_dpp v160, v160, v160 row_half_mirror row_mask:0xf bank_mask:0x5
	v_add_f32_dpp v160, v161, v161 row_half_mirror row_mask:0xf bank_mask:0xa
	v_add_f32_dpp v156, v156, v156 row_half_mirror row_mask:0xf bank_mask:0x5
	v_add_f32_dpp v156, v157, v157 row_half_mirror row_mask:0xf bank_mask:0xa
	v_add_f32_dpp v222, v222, v222 row_ror:8 row_mask:0xf bank_mask:0x3
	v_add_f32_dpp v222, v220, v220 row_ror:8 row_mask:0xf bank_mask:0xc
	v_add_f32_dpp v218, v218, v218 row_ror:8 row_mask:0xf bank_mask:0x3
	v_add_f32_dpp v218, v216, v216 row_ror:8 row_mask:0xf bank_mask:0xc
	v_add_f32_dpp v214, v214, v214 row_ror:8 row_mask:0xf bank_mask:0x3
	v_add_f32_dpp v214, v204, v204 row_ror:8 row_mask:0xf bank_mask:0xc
	v_add_f32_dpp v202, v202, v202 row_ror:8 row_mask:0xf bank_mask:0x3
	v_add_f32_dpp v202, v196, v196 row_ror:8 row_mask:0xf bank_mask:0xc
	v_add_f32_dpp v194, v194, v194 row_ror:8 row_mask:0xf bank_mask:0x3
	v_add_f32_dpp v194, v192, v192 row_ror:8 row_mask:0xf bank_mask:0xc
	v_add_f32_dpp v184, v184, v184 row_ror:8 row_mask:0xf bank_mask:0x3
	v_add_f32_dpp v184, v166, v166 row_ror:8 row_mask:0xf bank_mask:0xc
	v_add_f32_dpp v164, v164, v164 row_ror:8 row_mask:0xf bank_mask:0x3
	v_add_f32_dpp v164, v162, v162 row_ror:8 row_mask:0xf bank_mask:0xc
	v_add_f32_dpp v160, v160, v160 row_ror:8 row_mask:0xf bank_mask:0x3
	v_add_f32_dpp v160, v156, v156 row_ror:8 row_mask:0xf bank_mask:0xc
	v_add_f32_dpp v222, v222, v222 quad_perm:[1,0,3,2] row_mask:0xf bank_mask:0xf
	v_add_f32_dpp v218, v218, v218 quad_perm:[1,0,3,2] row_mask:0xf bank_mask:0xf
	v_add_f32_dpp v214, v214, v214 quad_perm:[1,0,3,2] row_mask:0xf bank_mask:0xf
	v_add_f32_dpp v202, v202, v202 quad_perm:[1,0,3,2] row_mask:0xf bank_mask:0xf
	v_add_f32_dpp v194, v194, v194 quad_perm:[1,0,3,2] row_mask:0xf bank_mask:0xf
	v_add_f32_dpp v184, v184, v184 quad_perm:[1,0,3,2] row_mask:0xf bank_mask:0xf
	v_add_f32_dpp v164, v164, v164 quad_perm:[1,0,3,2] row_mask:0xf bank_mask:0xf
	v_add_f32_dpp v160, v160, v160 quad_perm:[1,0,3,2] row_mask:0xf bank_mask:0xf
	v_add_f32_dpp v222, v222, v222 quad_perm:[2,3,0,1] row_mask:0xf bank_mask:0xf
	v_add_f32_dpp v218, v218, v218 quad_perm:[2,3,0,1] row_mask:0xf bank_mask:0xf
	v_add_f32_dpp v214, v214, v214 quad_perm:[2,3,0,1] row_mask:0xf bank_mask:0xf
	v_add_f32_dpp v202, v202, v202 quad_perm:[2,3,0,1] row_mask:0xf bank_mask:0xf
	v_add_f32_dpp v194, v194, v194 quad_perm:[2,3,0,1] row_mask:0xf bank_mask:0xf
	v_add_f32_dpp v184, v184, v184 quad_perm:[2,3,0,1] row_mask:0xf bank_mask:0xf
	v_add_f32_dpp v164, v164, v164 quad_perm:[2,3,0,1] row_mask:0xf bank_mask:0xf
	v_add_f32_dpp v160, v160, v160 quad_perm:[2,3,0,1] row_mask:0xf bank_mask:0xf
	s_mov_b32 exec_lo, 0x11111111
	s_mov_b32 exec_hi, 0x11111111
	ds_add_f32 v250, v222 offset:0
	ds_add_f32 v250, v218 offset:32
	ds_add_f32 v250, v214 offset:64
	ds_add_f32 v250, v202 offset:96
	ds_add_f32 v250, v194 offset:256
	ds_add_f32 v250, v184 offset:288
	ds_add_f32 v250, v164 offset:320
	ds_add_f32 v250, v160 offset:352
	s_mov_b64 exec, -1
	s_waitcnt lgkmcnt(0)
	s_barrier

.LBB3_24:
	s_or_b64 exec, exec, s[2:3]
	v_and_b32_e32 v1, 31, v0
	v_lshlrev_b32_e32 v2, 2, v1
	v_lshl_or_b32 v2, s13, 7, v2
	v_or_b32_e32 v2, 0x1ee00, v2
	v_lshrrev_b32_e32 v158, 5, v156
	s_waitcnt lgkmcnt(0)
	s_barrier
	v_lshlrev_b32_e32 v250, 4, v158
	v_lshl_or_b32 v250, s13, 7, v250
	v_or_b32_e32 v254, 0x1ee00, v250
	ds_read_b128 v[168:171], v254 offset:0
	ds_read_b128 v[172:175], v254 offset:32
	ds_read_b128 v[176:179], v254 offset:64
	ds_read_b128 v[180:183], v254 offset:96
	v_bfe_u32 v255, v156, 2, 2
	v_lshl_add_u32 v250, v255, 2, v250
	v_add_u32_e32 v250, 0x1e400, v250
	s_waitcnt lgkmcnt(0)
	s_barrier
	ds_read_b32 v157, v2
	v_mul_u32_u24_e32 v2, 0x88, v1
	s_mul_i32 s0, s16, 0x4400
	v_lshlrev_b32_e32 v2, 1, v2
	v_lshlrev_b32_e32 v3, 4, v158
	v_mov_b32_e32 v138, v0
	v_add3_u32 v159, s0, v2, v3
	ds_read_b128 v[2:5], v159
	ds_read_b128 v[18:21], v159 offset:8704
	ds_read_b128 v[130:133], v159 offset:32
	s_waitcnt vmcnt(10) lgkmcnt(2)
	v_mfma_f32_32x32x16_f16 v[50:65], v[2:5], v[126:129], 0
	s_mov_b32 s2, 0xc060c00
	s_mov_b32 s3, 0xe400
	s_mulk_i32 s16, 0x2400
	s_lshl_b32 s0, s13, 6
	s_or_b32 s0, s16, s0
	s_add_i32 s0, s0, 0x11000
	v_mul_u32_u24_e32 v251, 0x90, v1
	v_lshl_add_u32 v251, v158, 3, v251
	v_add_u32_e32 v251, s0, v251
	s_waitcnt lgkmcnt(1)
	v_mfma_f32_32x32x16_f16 v[34:49], v[18:21], v[126:129], 0
	s_or_b32 s0, s10, 2
	s_ashr_i32 s1, s0, 31
	s_lshl_b64 s[0:1], s[0:1], 12
	s_add_u32 s0, s8, s0
	s_addc_u32 s1, s9, s1
	v_cmp_gt_u32_e32 vcc, 32, v156
	v_mfma_f32_32x32x16_f16 v[2:17], v[122:125], v[2:5], v[168:183]
	v_mfma_f32_32x32x16_f16 v[18:33], v[122:125], v[18:21], v[168:183]
	ds_read_b128 v[134:137], v159 offset:8736
	ds_read_b128 v[160:163], v159 offset:64
	s_waitcnt vmcnt(8) lgkmcnt(2)
	v_mfma_f32_32x32x16_f16 v[50:65], v[130:133], v[118:121], v[50:65]
	s_waitcnt lgkmcnt(1)
	v_mfma_f32_32x32x16_f16 v[34:49], v[134:137], v[118:121], v[34:49]
	v_mfma_f32_32x32x16_f16 v[2:17], v[114:117], v[130:133], v[2:17]
	v_mfma_f32_32x32x16_f16 v[18:33], v[114:117], v[134:137], v[18:33]
	ds_read_b128 v[130:133], v159 offset:8768
	ds_read_b128 v[134:137], v159 offset:96
	s_waitcnt vmcnt(6) lgkmcnt(2)
	v_mfma_f32_32x32x16_f16 v[50:65], v[160:163], v[110:113], v[50:65]
	s_waitcnt lgkmcnt(1)
	v_mfma_f32_32x32x16_f16 v[34:49], v[130:133], v[110:113], v[34:49]
	v_mfma_f32_32x32x16_f16 v[2:17], v[106:109], v[160:163], v[2:17]
	v_mfma_f32_32x32x16_f16 v[18:33], v[106:109], v[130:133], v[18:33]
	ds_read_b128 v[130:133], v159 offset:8800
	ds_read_b128 v[160:163], v159 offset:128
	s_waitcnt vmcnt(4) lgkmcnt(2)
	v_mfma_f32_32x32x16_f16 v[50:65], v[134:137], v[102:105], v[50:65]
	s_waitcnt lgkmcnt(1)
	v_mfma_f32_32x32x16_f16 v[34:49], v[130:133], v[102:105], v[34:49]
	v_mfma_f32_32x32x16_f16 v[2:17], v[98:101], v[134:137], v[2:17]
	v_mfma_f32_32x32x16_f16 v[18:33], v[98:101], v[130:133], v[18:33]
	ds_read_b128 v[130:133], v159 offset:8832
	ds_read_b128 v[134:137], v159 offset:160
	s_waitcnt vmcnt(3) lgkmcnt(2)
	v_mfma_f32_32x32x16_f16 v[50:65], v[160:163], v[94:97], v[50:65]
	s_waitcnt lgkmcnt(1)
	v_mfma_f32_32x32x16_f16 v[34:49], v[130:133], v[94:97], v[34:49]
	v_mfma_f32_32x32x16_f16 v[2:17], v[86:89], v[160:163], v[2:17]
	v_mfma_f32_32x32x16_f16 v[18:33], v[86:89], v[130:133], v[18:33]
	ds_read_b128 v[130:133], v159 offset:8864
	ds_read_b128 v[160:163], v159 offset:192
	s_waitcnt vmcnt(2) lgkmcnt(2)
	v_mfma_f32_32x32x16_f16 v[50:65], v[134:137], v[90:93], v[50:65]
	s_waitcnt lgkmcnt(1)
	v_mfma_f32_32x32x16_f16 v[34:49], v[130:133], v[90:93], v[34:49]
	v_mfma_f32_32x32x16_f16 v[2:17], v[78:81], v[134:137], v[2:17]
	v_mfma_f32_32x32x16_f16 v[18:33], v[78:81], v[130:133], v[18:33]
	ds_read_b128 v[130:133], v159 offset:8896
	ds_read_b128 v[164:167], v159 offset:224
	s_waitcnt vmcnt(1) lgkmcnt(2)
	v_mfma_f32_32x32x16_f16 v[50:65], v[160:163], v[82:85], v[50:65]
	s_waitcnt lgkmcnt(1)
	v_mfma_f32_32x32x16_f16 v[34:49], v[130:133], v[82:85], v[34:49]
	v_mfma_f32_32x32x16_f16 v[2:17], v[70:73], v[160:163], v[2:17]
	v_mfma_f32_32x32x16_f16 v[18:33], v[70:73], v[130:133], v[18:33]
	v_lshlrev_b32_e32 v130, 3, v138
	v_and_b32_e32 v241, 0x1f8, v130
	global_load_dwordx2 v[138:139], v241, s[0:1]
	global_load_dwordx2 v[134:135], v241, s[0:1] offset:512
	global_load_dwordx2 v[132:133], v241, s[0:1] offset:1024
	global_load_dwordx2 v[130:131], v241, s[0:1] offset:1536
	global_load_dwordx2 v[136:137], v241, s[0:1] offset:2048
	s_waitcnt vmcnt(5) lgkmcnt(0)
	v_mfma_f32_32x32x16_f16 v[50:65], v[164:167], v[74:77], v[50:65]
	v_mfma_f32_32x32x16_f16 v[2:17], v[66:69], v[164:167], v[2:17]
	s_nop 10
	v_cvt_pk_f16_f32 v57, v56, v57
	v_cvt_pk_f16_f32 v56, v54, v55
	v_cvt_pk_f16_f32 v55, v52, v53
	v_cvt_pk_f16_f32 v54, v50, v51
	v_perm_b32 v50, v240, v154, s42
	v_perm_b32 v51, v240, v154, s43
	v_perm_b32 v52, v240, v155, s42
	v_perm_b32 v53, v240, v155, s43
	v_pk_add_f16 v50, v50, s3 op_sel_hi:[1,0]
	v_pk_add_f16 v51, v51, s3 op_sel_hi:[1,0]
	v_pk_add_f16 v52, v52, s3 op_sel_hi:[1,0]
	v_pk_add_f16 v53, v53, s3 op_sel_hi:[1,0]
	v_cvt_pk_f16_f32 v65, v64, v65
	v_cvt_pk_f16_f32 v64, v62, v63
	v_cvt_pk_f16_f32 v63, v60, v61
	v_cvt_pk_f16_f32 v62, v58, v59
	v_mfma_f32_32x32x16_f16 v[2:17], v[54:57], v[50:53], v[2:17]
	v_perm_b32 v58, v240, v150, s42
	v_perm_b32 v59, v240, v150, s43
	v_perm_b32 v60, v240, v151, s42
	v_perm_b32 v61, v240, v151, s43
	v_pk_add_f16 v58, v58, s3 op_sel_hi:[1,0]
	v_pk_add_f16 v59, v59, s3 op_sel_hi:[1,0]
	v_pk_add_f16 v60, v60, s3 op_sel_hi:[1,0]
	v_pk_add_f16 v61, v61, s3 op_sel_hi:[1,0]
	s_nop 1
	v_mfma_f32_32x32x16_f16 v[2:17], v[62:65], v[58:61], v[2:17]
	ds_read_b128 v[160:163], v159 offset:8928
	v_perm_b32 v155, v240, v152, s43
	v_perm_b32 v164, v240, v153, s42
	s_waitcnt lgkmcnt(0)
	v_mfma_f32_32x32x16_f16 v[18:33], v[66:69], v[160:163], v[18:33]
	v_perm_b32 v154, v240, v152, s42
	v_perm_b32 v165, v240, v153, s43
	v_pk_add_f16 v152, v154, s3 op_sel_hi:[1,0]
	v_pk_add_f16 v153, v155, s3 op_sel_hi:[1,0]
	v_pk_add_f16 v154, v164, s3 op_sel_hi:[1,0]
	v_pk_add_f16 v155, v165, s3 op_sel_hi:[1,0]
	v_mfma_f32_32x32x16_f16 v[34:49], v[160:163], v[74:77], v[34:49]
	v_perm_b32 v151, v240, v148, s43
	v_perm_b32 v164, v240, v149, s42
	v_mfma_f32_32x32x16_f16 v[18:33], v[54:57], v[152:155], v[18:33]
	v_perm_b32 v150, v240, v148, s42
	v_perm_b32 v165, v240, v149, s43
	v_pk_add_f16 v148, v150, s3 op_sel_hi:[1,0]
	v_pk_add_f16 v149, v151, s3 op_sel_hi:[1,0]
	v_pk_add_f16 v150, v164, s3 op_sel_hi:[1,0]
	v_pk_add_f16 v151, v165, s3 op_sel_hi:[1,0]
	s_nop 2
	v_cvt_pk_f16_f32 v41, v40, v41
	v_cvt_pk_f16_f32 v40, v38, v39
	v_cvt_pk_f16_f32 v38, v34, v35
	v_cvt_pk_f16_f32 v39, v36, v37
	v_mfma_f32_32x32x16_f16 v[18:33], v[62:65], v[148:151], v[18:33]
	v_perm_b32 v34, v240, v146, s42
	v_perm_b32 v35, v240, v146, s43
	v_perm_b32 v36, v240, v147, s42
	v_perm_b32 v37, v240, v147, s43
	v_pk_add_f16 v34, v34, s3 op_sel_hi:[1,0]
	v_pk_add_f16 v35, v35, s3 op_sel_hi:[1,0]
	v_pk_add_f16 v36, v36, s3 op_sel_hi:[1,0]
	v_pk_add_f16 v37, v37, s3 op_sel_hi:[1,0]
	v_perm_b32 v146, v240, v144, s42
	v_perm_b32 v144, v240, v144, s43
	v_perm_b32 v147, v240, v145, s42
	v_perm_b32 v53, v240, v145, s43
	v_pk_add_f16 v50, v146, s3 op_sel_hi:[1,0]
	v_pk_add_f16 v51, v144, s3 op_sel_hi:[1,0]
	v_pk_add_f16 v52, v147, s3 op_sel_hi:[1,0]
	v_pk_add_f16 v53, v53, s3 op_sel_hi:[1,0]
	v_cvt_pk_f16_f32 v49, v48, v49
	v_cvt_pk_f16_f32 v48, v46, v47
	v_cvt_pk_f16_f32 v47, v44, v45
	v_mfma_f32_32x32x16_f16 v[2:17], v[38:41], v[34:37], v[2:17]
	v_cvt_pk_f16_f32 v46, v42, v43
	v_mfma_f32_32x32x16_f16 v[18:33], v[38:41], v[50:53], v[18:33]
	v_perm_b32 v34, v240, v140, s42
	v_perm_b32 v35, v240, v140, s43
	v_perm_b32 v36, v240, v141, s42
	v_perm_b32 v37, v240, v141, s43
	v_perm_b32 v42, v240, v142, s42
	v_perm_b32 v43, v240, v142, s43
	v_perm_b32 v44, v240, v143, s42
	v_perm_b32 v45, v240, v143, s43
	v_pk_add_f16 v34, v34, s3 op_sel_hi:[1,0]
	v_pk_add_f16 v35, v35, s3 op_sel_hi:[1,0]
	v_pk_add_f16 v36, v36, s3 op_sel_hi:[1,0]
	v_pk_add_f16 v37, v37, s3 op_sel_hi:[1,0]
	v_pk_add_f16 v42, v42, s3 op_sel_hi:[1,0]
	v_pk_add_f16 v43, v43, s3 op_sel_hi:[1,0]
	v_pk_add_f16 v44, v44, s3 op_sel_hi:[1,0]
	v_pk_add_f16 v45, v45, s3 op_sel_hi:[1,0]
	v_mfma_f32_32x32x16_f16 v[18:33], v[46:49], v[34:37], v[18:33]
	global_load_dwordx2 v[154:155], v241, s[0:1] offset:2560
	global_load_dwordx2 v[152:153], v241, s[0:1] offset:3072
	global_load_dwordx2 v[150:151], v241, s[0:1] offset:3584
	v_mov_b32_e32 v148, v0
	s_or_b32 s0, s10, 4
	s_ashr_i32 s1, s0, 31
	s_lshl_b64 s[0:1], s[0:1], 12
	v_mfma_f32_32x32x16_f16 v[2:17], v[46:49], v[42:45], v[2:17]
	s_nop 7
	s_nop 4
	v_cvt_pk_f16_f32 v254, v2, v3
	v_cvt_pk_f16_f32 v255, v4, v5
	ds_write_b64 v251, v[254:255] offset:0
	v_mov_b32_e32 v222, v2
	v_mov_b32_e32 v223, v3
	v_pk_mul_f32 v[194:195], v[2:3], v[2:3]
	v_mov_b32_e32 v220, v4
	v_mov_b32_e32 v221, v5
	v_pk_mul_f32 v[192:193], v[4:5], v[4:5]
	v_cvt_pk_f16_f32 v252, v6, v7
	v_cvt_pk_f16_f32 v253, v8, v9
	ds_write_b64 v251, v[252:253] offset:16
	v_mov_b32_e32 v218, v6
	v_mov_b32_e32 v219, v7
	v_pk_mul_f32 v[184:185], v[6:7], v[6:7]
	v_mov_b32_e32 v216, v8
	v_mov_b32_e32 v217, v9
	v_pk_mul_f32 v[166:167], v[8:9], v[8:9]
	v_cvt_pk_f16_f32 v254, v10, v11
	v_cvt_pk_f16_f32 v255, v12, v13
	ds_write_b64 v251, v[254:255] offset:32
	v_mov_b32_e32 v214, v10
	v_mov_b32_e32 v215, v11
	v_pk_mul_f32 v[164:165], v[10:11], v[10:11]
	v_mov_b32_e32 v204, v12
	v_mov_b32_e32 v205, v13
	v_pk_mul_f32 v[162:163], v[12:13], v[12:13]
	v_cvt_pk_f16_f32 v252, v14, v15
	v_cvt_pk_f16_f32 v253, v16, v17
	ds_write_b64 v251, v[252:253] offset:48
	v_mov_b32_e32 v202, v14
	v_mov_b32_e32 v203, v15
	v_pk_mul_f32 v[160:161], v[14:15], v[14:15]
	v_mov_b32_e32 v196, v16
	v_mov_b32_e32 v197, v17
	v_pk_mul_f32 v[156:157], v[16:17], v[16:17]
	v_cvt_pk_f16_f32 v254, v18, v19
	v_cvt_pk_f16_f32 v255, v20, v21
	ds_write_b64 v251, v[254:255] offset:4608
	v_pk_add_f32 v[222:223], v[222:223], v[18:19]
	v_pk_fma_f32 v[194:195], v[18:19], v[18:19], v[194:195]
	v_pk_add_f32 v[220:221], v[220:221], v[20:21]
	v_pk_fma_f32 v[192:193], v[20:21], v[20:21], v[192:193]
	v_cvt_pk_f16_f32 v252, v22, v23
	v_cvt_pk_f16_f32 v253, v24, v25
	ds_write_b64 v251, v[252:253] offset:4624
	v_pk_add_f32 v[218:219], v[218:219], v[22:23]
	v_pk_fma_f32 v[184:185], v[22:23], v[22:23], v[184:185]
	v_pk_add_f32 v[216:217], v[216:217], v[24:25]
	v_pk_fma_f32 v[166:167], v[24:25], v[24:25], v[166:167]
	v_cvt_pk_f16_f32 v254, v26, v27
	v_cvt_pk_f16_f32 v255, v28, v29
	ds_write_b64 v251, v[254:255] offset:4640
	v_pk_add_f32 v[214:215], v[214:215], v[26:27]
	v_pk_fma_f32 v[164:165], v[26:27], v[26:27], v[164:165]
	v_pk_add_f32 v[204:205], v[204:205], v[28:29]
	v_pk_fma_f32 v[162:163], v[28:29], v[28:29], v[162:163]
	v_cvt_pk_f16_f32 v252, v30, v31
	v_cvt_pk_f16_f32 v253, v32, v33
	ds_write_b64 v251, v[252:253] offset:4656
	v_pk_add_f32 v[202:203], v[202:203], v[30:31]
	v_pk_fma_f32 v[160:161], v[30:31], v[30:31], v[160:161]
	v_pk_add_f32 v[196:197], v[196:197], v[32:33]
	v_pk_fma_f32 v[156:157], v[32:33], v[32:33], v[156:157]
	s_nop 3
	s_nop 0
	s_waitcnt lgkmcnt(0)
	s_barrier
	s_nop 4
	ds_read_b128 v[2:5], v159 offset:34816
	ds_read_b128 v[18:21], v159 offset:43520
	ds_read_b128 v[140:143], v159 offset:34848
	ds_read_b128 v[144:147], v159 offset:43552
	s_waitcnt lgkmcnt(3)
	v_mfma_f32_32x32x16_f16 v[50:65], v[2:5], v[126:129], 0
	s_add_u32 s0, s8, s0
	s_addc_u32 s1, s9, s1
	s_waitcnt lgkmcnt(2)
	v_mfma_f32_32x32x16_f16 v[34:49], v[18:21], v[126:129], 0
	v_mfma_f32_32x32x16_f16 v[2:17], v[122:125], v[2:5], v[168:183]
	v_mfma_f32_32x32x16_f16 v[18:33], v[122:125], v[18:21], v[168:183]
	ds_read_b128 v[242:245], v159 offset:34880
	ds_read_b128 v[246:249], v159 offset:43584
	s_waitcnt lgkmcnt(3)
	v_mfma_f32_32x32x16_f16 v[50:65], v[140:143], v[118:121], v[50:65]
	s_waitcnt lgkmcnt(2)
	v_mfma_f32_32x32x16_f16 v[34:49], v[144:147], v[118:121], v[34:49]
	v_mfma_f32_32x32x16_f16 v[2:17], v[114:117], v[140:143], v[2:17]
	v_mfma_f32_32x32x16_f16 v[18:33], v[114:117], v[144:147], v[18:33]
	ds_read_b128 v[140:143], v159 offset:34912
	ds_read_b128 v[144:147], v159 offset:43616
	s_waitcnt lgkmcnt(3)
	v_mfma_f32_32x32x16_f16 v[50:65], v[242:245], v[110:113], v[50:65]
	s_waitcnt lgkmcnt(2)
	v_mfma_f32_32x32x16_f16 v[34:49], v[246:249], v[110:113], v[34:49]
	v_mfma_f32_32x32x16_f16 v[2:17], v[106:109], v[242:245], v[2:17]
	v_mfma_f32_32x32x16_f16 v[18:33], v[106:109], v[246:249], v[18:33]
	ds_read_b128 v[242:245], v159 offset:34944
	ds_read_b128 v[246:249], v159 offset:43648
	s_waitcnt lgkmcnt(3)
	v_mfma_f32_32x32x16_f16 v[50:65], v[140:143], v[102:105], v[50:65]
	s_waitcnt lgkmcnt(2)
	v_mfma_f32_32x32x16_f16 v[34:49], v[144:147], v[102:105], v[34:49]
	v_mfma_f32_32x32x16_f16 v[2:17], v[98:101], v[140:143], v[2:17]
	v_mfma_f32_32x32x16_f16 v[18:33], v[98:101], v[144:147], v[18:33]
	ds_read_b128 v[186:189], v159 offset:34976
	ds_read_b128 v[206:209], v159 offset:43680
	s_waitcnt lgkmcnt(3)
	v_mfma_f32_32x32x16_f16 v[50:65], v[242:245], v[94:97], v[50:65]
	s_waitcnt lgkmcnt(2)
	v_mfma_f32_32x32x16_f16 v[34:49], v[246:249], v[94:97], v[34:49]
	v_mfma_f32_32x32x16_f16 v[2:17], v[86:89], v[242:245], v[2:17]
	v_mfma_f32_32x32x16_f16 v[18:33], v[86:89], v[246:249], v[18:33]
	ds_read_b128 v[140:143], v159 offset:35008
	ds_read_b128 v[144:147], v159 offset:43712
	s_waitcnt lgkmcnt(3)
	v_mfma_f32_32x32x16_f16 v[50:65], v[186:189], v[90:93], v[50:65]
	s_waitcnt lgkmcnt(2)
	v_mfma_f32_32x32x16_f16 v[34:49], v[206:209], v[90:93], v[34:49]
	v_mfma_f32_32x32x16_f16 v[2:17], v[78:81], v[186:189], v[2:17]
	v_mfma_f32_32x32x16_f16 v[18:33], v[78:81], v[206:209], v[18:33]
	ds_read_b128 v[186:189], v159 offset:35040
	ds_read_b128 v[206:209], v159 offset:43744
	s_waitcnt lgkmcnt(3)
	v_mfma_f32_32x32x16_f16 v[50:65], v[140:143], v[82:85], v[50:65]
	s_waitcnt lgkmcnt(2)
	v_mfma_f32_32x32x16_f16 v[34:49], v[144:147], v[82:85], v[34:49]
	v_mfma_f32_32x32x16_f16 v[2:17], v[70:73], v[140:143], v[2:17]
	v_lshlrev_b32_e32 v140, 3, v148
	v_and_b32_e32 v199, 0x1f8, v140
	global_load_dwordx2 v[148:149], v199, s[0:1]
	global_load_dwordx2 v[142:143], v199, s[0:1] offset:1024
	global_load_dwordx2 v[140:141], v199, s[0:1] offset:1536
	v_mfma_f32_32x32x16_f16 v[18:33], v[70:73], v[144:147], v[18:33]
	global_load_dwordx2 v[144:145], v199, s[0:1] offset:512
	global_load_dwordx2 v[146:147], v199, s[0:1] offset:2048
	s_waitcnt lgkmcnt(1)
	v_mfma_f32_32x32x16_f16 v[50:65], v[186:189], v[74:77], v[50:65]
	v_mfma_f32_32x32x16_f16 v[2:17], v[66:69], v[186:189], v[2:17]
	s_nop 10
	v_cvt_pk_f16_f32 v57, v56, v57
	v_cvt_pk_f16_f32 v56, v54, v55
	v_cvt_pk_f16_f32 v54, v50, v51
	s_waitcnt vmcnt(12)
	v_cvt_pk_f16_f32 v55, v52, v53
	s_waitcnt vmcnt(8)
	v_perm_b32 v50, v240, v138, s42
	v_perm_b32 v51, v240, v138, s43
	v_perm_b32 v52, v240, v139, s42
	v_perm_b32 v53, v240, v139, s43
	v_perm_b32 v139, v240, v136, s43
	v_pk_add_f16 v50, v50, s3 op_sel_hi:[1,0]
	v_pk_add_f16 v51, v51, s3 op_sel_hi:[1,0]
	v_pk_add_f16 v52, v52, s3 op_sel_hi:[1,0]
	v_pk_add_f16 v53, v53, s3 op_sel_hi:[1,0]
	v_perm_b32 v190, v240, v137, s42
	s_waitcnt lgkmcnt(0)
	v_mfma_f32_32x32x16_f16 v[18:33], v[66:69], v[206:209], v[18:33]
	v_perm_b32 v138, v240, v136, s42
	v_perm_b32 v191, v240, v137, s43
	v_pk_add_f16 v136, v138, s3 op_sel_hi:[1,0]
	v_pk_add_f16 v137, v139, s3 op_sel_hi:[1,0]
	v_pk_add_f16 v138, v190, s3 op_sel_hi:[1,0]
	v_pk_add_f16 v139, v191, s3 op_sel_hi:[1,0]
	v_cvt_pk_f16_f32 v65, v64, v65
	v_cvt_pk_f16_f32 v64, v62, v63
	v_cvt_pk_f16_f32 v63, v60, v61
	v_cvt_pk_f16_f32 v62, v58, v59
	v_mfma_f32_32x32x16_f16 v[34:49], v[206:209], v[74:77], v[34:49]
	v_mfma_f32_32x32x16_f16 v[2:17], v[54:57], v[50:53], v[2:17]
	s_waitcnt vmcnt(7)
	v_perm_b32 v58, v240, v134, s42
	v_perm_b32 v59, v240, v134, s43
	v_perm_b32 v60, v240, v135, s42
	v_perm_b32 v61, v240, v135, s43
	v_pk_add_f16 v58, v58, s3 op_sel_hi:[1,0]
	v_pk_add_f16 v59, v59, s3 op_sel_hi:[1,0]
	v_pk_add_f16 v60, v60, s3 op_sel_hi:[1,0]
	v_pk_add_f16 v61, v61, s3 op_sel_hi:[1,0]
	v_mfma_f32_32x32x16_f16 v[18:33], v[54:57], v[136:139], v[18:33]
	v_perm_b32 v134, v240, v154, s42
	v_perm_b32 v135, v240, v154, s43
	v_perm_b32 v154, v240, v155, s42
	v_perm_b32 v155, v240, v155, s43
	v_pk_add_f16 v210, v134, s3 op_sel_hi:[1,0]
	v_pk_add_f16 v211, v135, s3 op_sel_hi:[1,0]
	v_pk_add_f16 v212, v154, s3 op_sel_hi:[1,0]
	v_pk_add_f16 v213, v155, s3 op_sel_hi:[1,0]
	v_cvt_pk_f16_f32 v41, v40, v41
	v_cvt_pk_f16_f32 v40, v38, v39
	v_cvt_pk_f16_f32 v39, v36, v37
	v_cvt_pk_f16_f32 v38, v34, v35
	v_mfma_f32_32x32x16_f16 v[2:17], v[62:65], v[58:61], v[2:17]
	v_perm_b32 v34, v240, v132, s42
	v_perm_b32 v35, v240, v132, s43
	v_perm_b32 v36, v240, v133, s42
	v_perm_b32 v37, v240, v133, s43
	v_pk_add_f16 v34, v34, s3 op_sel_hi:[1,0]
	v_pk_add_f16 v35, v35, s3 op_sel_hi:[1,0]
	v_pk_add_f16 v36, v36, s3 op_sel_hi:[1,0]
	v_pk_add_f16 v37, v37, s3 op_sel_hi:[1,0]
	s_waitcnt vmcnt(6)
	v_mfma_f32_32x32x16_f16 v[18:33], v[62:65], v[210:213], v[18:33]
	v_perm_b32 v132, v240, v152, s42
	v_perm_b32 v133, v240, v152, s43
	v_perm_b32 v134, v240, v153, s42
	v_perm_b32 v53, v240, v153, s43
	v_pk_add_f16 v50, v132, s3 op_sel_hi:[1,0]
	v_pk_add_f16 v51, v133, s3 op_sel_hi:[1,0]
	v_pk_add_f16 v52, v134, s3 op_sel_hi:[1,0]
	v_pk_add_f16 v53, v53, s3 op_sel_hi:[1,0]
	v_cvt_pk_f16_f32 v49, v48, v49
	v_cvt_pk_f16_f32 v48, v46, v47
	v_cvt_pk_f16_f32 v47, v44, v45
	v_cvt_pk_f16_f32 v46, v42, v43
	v_mfma_f32_32x32x16_f16 v[2:17], v[38:41], v[34:37], v[2:17]
	v_perm_b32 v42, v240, v130, s42
	v_perm_b32 v43, v240, v130, s43
	v_perm_b32 v44, v240, v131, s42
	v_perm_b32 v45, v240, v131, s43
	v_pk_add_f16 v42, v42, s3 op_sel_hi:[1,0]
	v_pk_add_f16 v43, v43, s3 op_sel_hi:[1,0]
	v_pk_add_f16 v44, v44, s3 op_sel_hi:[1,0]
	v_pk_add_f16 v45, v45, s3 op_sel_hi:[1,0]
	s_waitcnt vmcnt(5)
	v_mfma_f32_32x32x16_f16 v[18:33], v[38:41], v[50:53], v[18:33]
	v_perm_b32 v34, v240, v150, s42
	v_perm_b32 v35, v240, v150, s43
	v_perm_b32 v36, v240, v151, s42
	v_perm_b32 v37, v240, v151, s43
	v_pk_add_f16 v34, v34, s3 op_sel_hi:[1,0]
	v_pk_add_f16 v35, v35, s3 op_sel_hi:[1,0]
	v_pk_add_f16 v36, v36, s3 op_sel_hi:[1,0]
	v_pk_add_f16 v37, v37, s3 op_sel_hi:[1,0]
	v_mfma_f32_32x32x16_f16 v[2:17], v[46:49], v[42:45], v[2:17]
	global_load_dwordx2 v[154:155], v199, s[0:1] offset:2560
	global_load_dwordx2 v[152:153], v199, s[0:1] offset:3072
	global_load_dwordx2 v[150:151], v199, s[0:1] offset:3584
	s_or_b32 s0, s10, 6
	s_ashr_i32 s1, s0, 31
	s_lshl_b64 s[0:1], s[0:1], 12
	s_add_u32 s0, s8, s0
	v_mfma_f32_32x32x16_f16 v[18:33], v[46:49], v[34:37], v[18:33]
	s_nop 7
	s_nop 4
	v_cvt_pk_f16_f32 v254, v2, v3
	v_cvt_pk_f16_f32 v255, v4, v5
	ds_write_b64 v251, v[254:255] offset:18432
	v_pk_add_f32 v[222:223], v[222:223], v[2:3]
	v_pk_fma_f32 v[194:195], v[2:3], v[2:3], v[194:195]
	v_pk_add_f32 v[220:221], v[220:221], v[4:5]
	v_pk_fma_f32 v[192:193], v[4:5], v[4:5], v[192:193]
	v_cvt_pk_f16_f32 v252, v6, v7
	v_cvt_pk_f16_f32 v253, v8, v9
	ds_write_b64 v251, v[252:253] offset:18448
	v_pk_add_f32 v[218:219], v[218:219], v[6:7]
	v_pk_fma_f32 v[184:185], v[6:7], v[6:7], v[184:185]
	v_pk_add_f32 v[216:217], v[216:217], v[8:9]
	v_pk_fma_f32 v[166:167], v[8:9], v[8:9], v[166:167]
	v_cvt_pk_f16_f32 v254, v10, v11
	v_cvt_pk_f16_f32 v255, v12, v13
	ds_write_b64 v251, v[254:255] offset:18464
	v_pk_add_f32 v[214:215], v[214:215], v[10:11]
	v_pk_fma_f32 v[164:165], v[10:11], v[10:11], v[164:165]
	v_pk_add_f32 v[204:205], v[204:205], v[12:13]
	v_pk_fma_f32 v[162:163], v[12:13], v[12:13], v[162:163]
	v_cvt_pk_f16_f32 v252, v14, v15
	v_cvt_pk_f16_f32 v253, v16, v17
	ds_write_b64 v251, v[252:253] offset:18480
	v_pk_add_f32 v[202:203], v[202:203], v[14:15]
	v_pk_fma_f32 v[160:161], v[14:15], v[14:15], v[160:161]
	v_pk_add_f32 v[196:197], v[196:197], v[16:17]
	v_pk_fma_f32 v[156:157], v[16:17], v[16:17], v[156:157]
	v_cvt_pk_f16_f32 v254, v18, v19
	v_cvt_pk_f16_f32 v255, v20, v21
	ds_write_b64 v251, v[254:255] offset:23040
	v_pk_add_f32 v[222:223], v[222:223], v[18:19]
	v_pk_fma_f32 v[194:195], v[18:19], v[18:19], v[194:195]
	v_pk_add_f32 v[220:221], v[220:221], v[20:21]
	v_pk_fma_f32 v[192:193], v[20:21], v[20:21], v[192:193]
	v_cvt_pk_f16_f32 v252, v22, v23
	v_cvt_pk_f16_f32 v253, v24, v25
	ds_write_b64 v251, v[252:253] offset:23056
	v_pk_add_f32 v[218:219], v[218:219], v[22:23]
	v_pk_fma_f32 v[184:185], v[22:23], v[22:23], v[184:185]
	v_pk_add_f32 v[216:217], v[216:217], v[24:25]
	v_pk_fma_f32 v[166:167], v[24:25], v[24:25], v[166:167]
	v_cvt_pk_f16_f32 v254, v26, v27
	v_cvt_pk_f16_f32 v255, v28, v29
	ds_write_b64 v251, v[254:255] offset:23072
	v_pk_add_f32 v[214:215], v[214:215], v[26:27]
	v_pk_fma_f32 v[164:165], v[26:27], v[26:27], v[164:165]
	v_pk_add_f32 v[204:205], v[204:205], v[28:29]
	v_pk_fma_f32 v[162:163], v[28:29], v[28:29], v[162:163]
	v_cvt_pk_f16_f32 v252, v30, v31
	v_cvt_pk_f16_f32 v253, v32, v33
	ds_write_b64 v251, v[252:253] offset:23088
	v_pk_add_f32 v[202:203], v[202:203], v[30:31]
	v_pk_fma_f32 v[160:161], v[30:31], v[30:31], v[160:161]
	v_pk_add_f32 v[196:197], v[196:197], v[32:33]
	v_pk_fma_f32 v[156:157], v[32:33], v[32:33], v[156:157]
	s_nop 3
	s_nop 0
	s_nop 0
	s_waitcnt lgkmcnt(0)
	s_barrier
	ds_read_b128 v[2:5], v159
	s_nop 2
	ds_read_b128 v[18:21], v159 offset:8704
	s_waitcnt lgkmcnt(1)
	v_mfma_f32_32x32x16_f16 v[50:65], v[2:5], v[126:129], 0
	v_lshlrev_b32_e32 v0, 3, v0
	s_addc_u32 s1, s9, s1
	v_and_b32_e32 v0, 0x1f8, v0
	global_load_dwordx2 v[138:139], v0, s[0:1]
	s_waitcnt lgkmcnt(0)
	v_mfma_f32_32x32x16_f16 v[34:49], v[18:21], v[126:129], 0
	v_mfma_f32_32x32x16_f16 v[2:17], v[122:125], v[2:5], v[168:183]
	v_mfma_f32_32x32x16_f16 v[18:33], v[122:125], v[18:21], v[168:183]
	ds_read_b128 v[130:133], v159 offset:32
	ds_read_b128 v[134:137], v159 offset:8736
	s_waitcnt lgkmcnt(1)
	v_mfma_f32_32x32x16_f16 v[50:65], v[130:133], v[118:121], v[50:65]
	s_waitcnt lgkmcnt(0)
	v_mfma_f32_32x32x16_f16 v[34:49], v[134:137], v[118:121], v[34:49]
	v_mfma_f32_32x32x16_f16 v[2:17], v[114:117], v[130:133], v[2:17]
	v_mfma_f32_32x32x16_f16 v[18:33], v[114:117], v[134:137], v[18:33]
	ds_read_b128 v[224:227], v159 offset:64
	ds_read_b128 v[228:231], v159 offset:8768
	ds_read_b128 v[130:133], v159 offset:96
	ds_read_b128 v[134:137], v159 offset:8800
	s_waitcnt lgkmcnt(3)
	v_mfma_f32_32x32x16_f16 v[50:65], v[224:227], v[110:113], v[50:65]
	s_waitcnt lgkmcnt(2)
	v_mfma_f32_32x32x16_f16 v[34:49], v[228:231], v[110:113], v[34:49]
	v_mfma_f32_32x32x16_f16 v[2:17], v[106:109], v[224:227], v[2:17]
	v_mfma_f32_32x32x16_f16 v[18:33], v[106:109], v[228:231], v[18:33]
	ds_read_b128 v[224:227], v159 offset:128
	ds_read_b128 v[228:231], v159 offset:8832
	s_waitcnt lgkmcnt(3)
	v_mfma_f32_32x32x16_f16 v[50:65], v[130:133], v[102:105], v[50:65]
	s_waitcnt lgkmcnt(2)
	v_mfma_f32_32x32x16_f16 v[34:49], v[134:137], v[102:105], v[34:49]
	v_mfma_f32_32x32x16_f16 v[2:17], v[98:101], v[130:133], v[2:17]
	v_mfma_f32_32x32x16_f16 v[18:33], v[98:101], v[134:137], v[18:33]
	ds_read_b128 v[130:133], v159 offset:160
	ds_read_b128 v[134:137], v159 offset:8864
	s_waitcnt lgkmcnt(3)
	v_mfma_f32_32x32x16_f16 v[50:65], v[224:227], v[94:97], v[50:65]
	s_waitcnt lgkmcnt(2)
	v_mfma_f32_32x32x16_f16 v[34:49], v[228:231], v[94:97], v[34:49]
	v_mfma_f32_32x32x16_f16 v[2:17], v[86:89], v[224:227], v[2:17]
	v_mfma_f32_32x32x16_f16 v[18:33], v[86:89], v[228:231], v[18:33]
	ds_read_b128 v[224:227], v159 offset:192
	ds_read_b128 v[228:231], v159 offset:8896
	s_waitcnt lgkmcnt(3)
	v_mfma_f32_32x32x16_f16 v[50:65], v[130:133], v[90:93], v[50:65]
	s_waitcnt lgkmcnt(2)
	v_mfma_f32_32x32x16_f16 v[34:49], v[134:137], v[90:93], v[34:49]
	v_mfma_f32_32x32x16_f16 v[2:17], v[78:81], v[130:133], v[2:17]
	v_mfma_f32_32x32x16_f16 v[18:33], v[78:81], v[134:137], v[18:33]
	ds_read_b128 v[232:235], v159 offset:224
	ds_read_b128 v[236:239], v159 offset:8928
	s_waitcnt lgkmcnt(3)
	v_mfma_f32_32x32x16_f16 v[50:65], v[224:227], v[82:85], v[50:65]
	global_load_dwordx2 v[134:135], v0, s[0:1] offset:512
	global_load_dwordx2 v[132:133], v0, s[0:1] offset:1024
	global_load_dwordx2 v[130:131], v0, s[0:1] offset:1536
	s_waitcnt lgkmcnt(2)
	v_mfma_f32_32x32x16_f16 v[34:49], v[228:231], v[82:85], v[34:49]
	global_load_dwordx2 v[136:137], v0, s[0:1] offset:2048
	v_mfma_f32_32x32x16_f16 v[2:17], v[70:73], v[224:227], v[2:17]
	v_mfma_f32_32x32x16_f16 v[18:33], v[70:73], v[228:231], v[18:33]
	s_waitcnt lgkmcnt(1)
	v_mfma_f32_32x32x16_f16 v[50:65], v[232:235], v[74:77], v[50:65]
	v_mfma_f32_32x32x16_f16 v[2:17], v[66:69], v[232:235], v[2:17]
	s_nop 10
	v_cvt_pk_f16_f32 v57, v56, v57
	v_cvt_pk_f16_f32 v56, v54, v55
	v_cvt_pk_f16_f32 v54, v50, v51
	s_waitcnt vmcnt(12)
	v_lshlrev_b32_e32 v50, 8, v148
	v_cvt_pk_f16_f32 v55, v52, v53
	v_perm_b32 v50, v50, v148, s2
	v_lshrrev_b32_e32 v51, 16, v148
	v_lshrrev_b32_e32 v52, 8, v148
	v_lshrrev_b32_e32 v53, 16, v149
	v_lshrrev_b32_e32 v148, 8, v149
	v_perm_b32 v51, v52, v51, s2
	v_lshlrev_b32_e32 v52, 8, v149
	v_perm_b32 v53, v148, v53, s2
	s_waitcnt vmcnt(8)
	v_perm_b32 v52, v52, v149, s2
	v_perm_b32 v149, v240, v146, s43
	v_perm_b32 v198, v240, v147, s42
	s_waitcnt lgkmcnt(0)
	v_mfma_f32_32x32x16_f16 v[18:33], v[66:69], v[236:239], v[18:33]
	v_or_b32_e32 v50, 0x64006400, v50
	v_or_b32_e32 v51, 0x64006400, v51
	v_or_b32_e32 v52, 0x64006400, v52
	v_or_b32_e32 v53, 0x64006400, v53
	v_pk_add_f16 v50, v50, s3 op_sel_hi:[1,0]
	v_pk_add_f16 v51, v51, s3 op_sel_hi:[1,0]
	v_pk_add_f16 v52, v52, s3 op_sel_hi:[1,0]
	v_pk_add_f16 v53, v53, s3 op_sel_hi:[1,0]
	v_perm_b32 v148, v240, v146, s42
	v_perm_b32 v200, v240, v147, s43
	v_pk_add_f16 v146, v148, s3 op_sel_hi:[1,0]
	v_pk_add_f16 v147, v149, s3 op_sel_hi:[1,0]
	v_pk_add_f16 v148, v198, s3 op_sel_hi:[1,0]
	v_pk_add_f16 v149, v200, s3 op_sel_hi:[1,0]
	v_cvt_pk_f16_f32 v65, v64, v65
	v_cvt_pk_f16_f32 v64, v62, v63
	v_cvt_pk_f16_f32 v62, v58, v59
	v_cvt_pk_f16_f32 v63, v60, v61
	s_waitcnt vmcnt(7)
	v_mfma_f32_32x32x16_f16 v[34:49], v[236:239], v[74:77], v[34:49]
	v_mfma_f32_32x32x16_f16 v[2:17], v[54:57], v[50:53], v[2:17]
	v_perm_b32 v58, v240, v144, s42
	v_perm_b32 v59, v240, v144, s43
	v_perm_b32 v60, v240, v145, s42
	v_perm_b32 v61, v240, v145, s43
	v_mfma_f32_32x32x16_f16 v[18:33], v[54:57], v[146:149], v[18:33]
	v_pk_add_f16 v58, v58, s3 op_sel_hi:[1,0]
	v_pk_add_f16 v59, v59, s3 op_sel_hi:[1,0]
	v_pk_add_f16 v60, v60, s3 op_sel_hi:[1,0]
	v_pk_add_f16 v61, v61, s3 op_sel_hi:[1,0]
	v_perm_b32 v144, v240, v154, s42
	v_perm_b32 v145, v240, v154, s43
	v_perm_b32 v154, v240, v155, s42
	v_perm_b32 v155, v240, v155, s43
	v_pk_add_f16 v224, v144, s3 op_sel_hi:[1,0]
	v_pk_add_f16 v225, v145, s3 op_sel_hi:[1,0]
	v_pk_add_f16 v226, v154, s3 op_sel_hi:[1,0]
	v_pk_add_f16 v227, v155, s3 op_sel_hi:[1,0]
	v_cvt_pk_f16_f32 v41, v40, v41
	v_cvt_pk_f16_f32 v40, v38, v39
	v_cvt_pk_f16_f32 v39, v36, v37
	v_cvt_pk_f16_f32 v38, v34, v35
	s_waitcnt vmcnt(6)
	v_mfma_f32_32x32x16_f16 v[2:17], v[62:65], v[58:61], v[2:17]
	v_perm_b32 v34, v240, v142, s42
	v_perm_b32 v35, v240, v142, s43
	v_mfma_f32_32x32x16_f16 v[18:33], v[62:65], v[224:227], v[18:33]
	v_perm_b32 v36, v240, v143, s42
	v_perm_b32 v37, v240, v143, s43
	v_pk_add_f16 v34, v34, s3 op_sel_hi:[1,0]
	v_pk_add_f16 v35, v35, s3 op_sel_hi:[1,0]
	v_pk_add_f16 v36, v36, s3 op_sel_hi:[1,0]
	v_pk_add_f16 v37, v37, s3 op_sel_hi:[1,0]
	v_perm_b32 v142, v240, v152, s42
	v_perm_b32 v143, v240, v152, s43
	v_perm_b32 v144, v240, v153, s42
	v_perm_b32 v53, v240, v153, s43
	v_pk_add_f16 v50, v142, s3 op_sel_hi:[1,0]
	v_pk_add_f16 v51, v143, s3 op_sel_hi:[1,0]
	v_pk_add_f16 v52, v144, s3 op_sel_hi:[1,0]
	v_pk_add_f16 v53, v53, s3 op_sel_hi:[1,0]
	v_cvt_pk_f16_f32 v49, v48, v49
	v_cvt_pk_f16_f32 v48, v46, v47
	v_cvt_pk_f16_f32 v47, v44, v45
	v_cvt_pk_f16_f32 v46, v42, v43
	v_mfma_f32_32x32x16_f16 v[2:17], v[38:41], v[34:37], v[2:17]
	s_waitcnt vmcnt(5)
	v_mfma_f32_32x32x16_f16 v[18:33], v[38:41], v[50:53], v[18:33]
	v_perm_b32 v42, v240, v140, s42
	v_perm_b32 v43, v240, v140, s43
	v_perm_b32 v44, v240, v141, s42
	v_perm_b32 v45, v240, v141, s43
	v_perm_b32 v34, v240, v150, s42
	v_perm_b32 v35, v240, v150, s43
	v_perm_b32 v36, v240, v151, s42
	v_perm_b32 v37, v240, v151, s43
	v_pk_add_f16 v42, v42, s3 op_sel_hi:[1,0]
	v_pk_add_f16 v43, v43, s3 op_sel_hi:[1,0]
	v_pk_add_f16 v44, v44, s3 op_sel_hi:[1,0]
	v_pk_add_f16 v45, v45, s3 op_sel_hi:[1,0]
	v_pk_add_f16 v34, v34, s3 op_sel_hi:[1,0]
	v_pk_add_f16 v35, v35, s3 op_sel_hi:[1,0]
	v_pk_add_f16 v36, v36, s3 op_sel_hi:[1,0]
	v_pk_add_f16 v37, v37, s3 op_sel_hi:[1,0]
	v_mfma_f32_32x32x16_f16 v[2:17], v[46:49], v[42:45], v[2:17]
	global_load_dwordx2 v[142:143], v0, s[0:1] offset:2560
	global_load_dwordx2 v[140:141], v0, s[0:1] offset:3072
	global_load_dwordx2 v[64:65], v0, s[0:1] offset:3584
	v_mfma_f32_32x32x16_f16 v[18:33], v[46:49], v[34:37], v[18:33]
	s_nop 7
	s_nop 4
	v_cvt_pk_f16_f32 v254, v2, v3
	v_cvt_pk_f16_f32 v255, v4, v5
	ds_write_b64 v251, v[254:255] offset:0
	v_pk_add_f32 v[222:223], v[222:223], v[2:3]
	v_pk_fma_f32 v[194:195], v[2:3], v[2:3], v[194:195]
	v_pk_add_f32 v[220:221], v[220:221], v[4:5]
	v_pk_fma_f32 v[192:193], v[4:5], v[4:5], v[192:193]
	v_cvt_pk_f16_f32 v252, v6, v7
	v_cvt_pk_f16_f32 v253, v8, v9
	ds_write_b64 v251, v[252:253] offset:16
	v_pk_add_f32 v[218:219], v[218:219], v[6:7]
	v_pk_fma_f32 v[184:185], v[6:7], v[6:7], v[184:185]
	v_pk_add_f32 v[216:217], v[216:217], v[8:9]
	v_pk_fma_f32 v[166:167], v[8:9], v[8:9], v[166:167]
	v_cvt_pk_f16_f32 v254, v10, v11
	v_cvt_pk_f16_f32 v255, v12, v13
	ds_write_b64 v251, v[254:255] offset:32
	v_pk_add_f32 v[214:215], v[214:215], v[10:11]
	v_pk_fma_f32 v[164:165], v[10:11], v[10:11], v[164:165]
	v_pk_add_f32 v[204:205], v[204:205], v[12:13]
	v_pk_fma_f32 v[162:163], v[12:13], v[12:13], v[162:163]
	v_cvt_pk_f16_f32 v252, v14, v15
	v_cvt_pk_f16_f32 v253, v16, v17
	ds_write_b64 v251, v[252:253] offset:48
	v_pk_add_f32 v[202:203], v[202:203], v[14:15]
	v_pk_fma_f32 v[160:161], v[14:15], v[14:15], v[160:161]
	v_pk_add_f32 v[196:197], v[196:197], v[16:17]
	v_pk_fma_f32 v[156:157], v[16:17], v[16:17], v[156:157]
	v_cvt_pk_f16_f32 v254, v18, v19
	v_cvt_pk_f16_f32 v255, v20, v21
	ds_write_b64 v251, v[254:255] offset:4608
	v_pk_add_f32 v[222:223], v[222:223], v[18:19]
	v_pk_fma_f32 v[194:195], v[18:19], v[18:19], v[194:195]
	v_pk_add_f32 v[220:221], v[220:221], v[20:21]
	v_pk_fma_f32 v[192:193], v[20:21], v[20:21], v[192:193]
	v_cvt_pk_f16_f32 v252, v22, v23
	v_cvt_pk_f16_f32 v253, v24, v25
	ds_write_b64 v251, v[252:253] offset:4624
	v_pk_add_f32 v[218:219], v[218:219], v[22:23]
	v_pk_fma_f32 v[184:185], v[22:23], v[22:23], v[184:185]
	v_pk_add_f32 v[216:217], v[216:217], v[24:25]
	v_pk_fma_f32 v[166:167], v[24:25], v[24:25], v[166:167]
	v_cvt_pk_f16_f32 v254, v26, v27
	v_cvt_pk_f16_f32 v255, v28, v29
	ds_write_b64 v251, v[254:255] offset:4640
	v_pk_add_f32 v[214:215], v[214:215], v[26:27]
	v_pk_fma_f32 v[164:165], v[26:27], v[26:27], v[164:165]
	v_pk_add_f32 v[204:205], v[204:205], v[28:29]
	v_pk_fma_f32 v[162:163], v[28:29], v[28:29], v[162:163]
	v_cvt_pk_f16_f32 v252, v30, v31
	v_cvt_pk_f16_f32 v253, v32, v33
	ds_write_b64 v251, v[252:253] offset:4656
	v_pk_add_f32 v[202:203], v[202:203], v[30:31]
	v_pk_fma_f32 v[160:161], v[30:31], v[30:31], v[160:161]
	v_pk_add_f32 v[196:197], v[196:197], v[32:33]
	v_pk_fma_f32 v[156:157], v[32:33], v[32:33], v[156:157]
	s_nop 7
	s_waitcnt lgkmcnt(0)
	s_barrier
	s_nop 1
	ds_read_b128 v[16:19], v159 offset:43520
	s_waitcnt lgkmcnt(0)
	v_mfma_f32_32x32x16_f16 v[32:47], v[16:19], v[126:129], 0
	ds_read_b128 v[2:5], v159 offset:34816
	s_waitcnt lgkmcnt(0)
	v_mfma_f32_32x32x16_f16 v[48:63], v[2:5], v[126:129], 0
	ds_read_b128 v[126:129], v159 offset:34848
	s_waitcnt lgkmcnt(0)
	v_mfma_f32_32x32x16_f16 v[48:63], v[126:129], v[118:121], v[48:63]
	v_mfma_f32_32x32x16_f16 v[0:15], v[122:125], v[2:5], v[168:183]
	v_mfma_f32_32x32x16_f16 v[0:15], v[114:117], v[126:129], v[0:15]
	v_mfma_f32_32x32x16_f16 v[16:31], v[122:125], v[16:19], v[168:183]
	ds_read_b128 v[122:125], v159 offset:43552
	s_waitcnt lgkmcnt(0)
	v_mfma_f32_32x32x16_f16 v[32:47], v[122:125], v[118:121], v[32:47]
	v_mfma_f32_32x32x16_f16 v[16:31], v[114:117], v[122:125], v[16:31]
	ds_read_b128 v[118:121], v159 offset:34880
	ds_read_b128 v[114:117], v159 offset:43584
	s_waitcnt lgkmcnt(1)
	v_mfma_f32_32x32x16_f16 v[48:63], v[118:121], v[110:113], v[48:63]
	s_waitcnt lgkmcnt(0)
	v_mfma_f32_32x32x16_f16 v[32:47], v[114:117], v[110:113], v[32:47]
	v_mfma_f32_32x32x16_f16 v[0:15], v[106:109], v[118:121], v[0:15]
	ds_read_b128 v[110:113], v159 offset:34912
	v_mfma_f32_32x32x16_f16 v[16:31], v[106:109], v[114:117], v[16:31]
	ds_read_b128 v[106:109], v159 offset:43616
	s_waitcnt lgkmcnt(1)
	v_mfma_f32_32x32x16_f16 v[48:63], v[110:113], v[102:105], v[48:63]
	s_waitcnt lgkmcnt(0)
	v_mfma_f32_32x32x16_f16 v[32:47], v[106:109], v[102:105], v[32:47]
	v_mfma_f32_32x32x16_f16 v[0:15], v[98:101], v[110:113], v[0:15]
	ds_read_b128 v[102:105], v159 offset:34944
	v_mfma_f32_32x32x16_f16 v[16:31], v[98:101], v[106:109], v[16:31]
	ds_read_b128 v[98:101], v159 offset:43648
	s_waitcnt lgkmcnt(1)
	v_mfma_f32_32x32x16_f16 v[48:63], v[102:105], v[94:97], v[48:63]
	s_waitcnt lgkmcnt(0)
	v_mfma_f32_32x32x16_f16 v[32:47], v[98:101], v[94:97], v[32:47]
	v_mfma_f32_32x32x16_f16 v[0:15], v[86:89], v[102:105], v[0:15]
	ds_read_b128 v[94:97], v159 offset:34976
	v_mfma_f32_32x32x16_f16 v[16:31], v[86:89], v[98:101], v[16:31]
	ds_read_b128 v[86:89], v159 offset:43680
	s_waitcnt lgkmcnt(1)
	v_mfma_f32_32x32x16_f16 v[48:63], v[94:97], v[90:93], v[48:63]
	s_waitcnt lgkmcnt(0)
	v_mfma_f32_32x32x16_f16 v[32:47], v[86:89], v[90:93], v[32:47]
	v_mfma_f32_32x32x16_f16 v[0:15], v[78:81], v[94:97], v[0:15]
	ds_read_b128 v[90:93], v159 offset:35008
	v_mfma_f32_32x32x16_f16 v[16:31], v[78:81], v[86:89], v[16:31]
	ds_read_b128 v[78:81], v159 offset:43712
	s_waitcnt lgkmcnt(1)
	v_mfma_f32_32x32x16_f16 v[48:63], v[90:93], v[82:85], v[48:63]
	s_waitcnt lgkmcnt(0)
	v_mfma_f32_32x32x16_f16 v[32:47], v[78:81], v[82:85], v[32:47]
	v_mfma_f32_32x32x16_f16 v[0:15], v[70:73], v[90:93], v[0:15]
	ds_read_b128 v[82:85], v159 offset:35040
	v_mfma_f32_32x32x16_f16 v[16:31], v[70:73], v[78:81], v[16:31]
	ds_read_b128 v[70:73], v159 offset:43744
	s_waitcnt lgkmcnt(1)
	v_mfma_f32_32x32x16_f16 v[48:63], v[82:85], v[74:77], v[48:63]
	v_mfma_f32_32x32x16_f16 v[0:15], v[66:69], v[82:85], v[0:15]
	s_nop 3
	s_nop 6
	v_cvt_pk_f16_f32 v55, v54, v55
	v_cvt_pk_f16_f32 v54, v52, v53
	v_cvt_pk_f16_f32 v53, v50, v51
	v_cvt_pk_f16_f32 v52, v48, v49
	s_waitcnt vmcnt(3)
	s_waitcnt lgkmcnt(0)
	v_mfma_f32_32x32x16_f16 v[16:31], v[66:69], v[70:73], v[16:31]
	v_lshrrev_b32_e32 v69, 16, v139
	v_mfma_f32_32x32x16_f16 v[32:47], v[70:73], v[74:77], v[32:47]
	v_lshrrev_b32_e32 v70, 8, v139
	v_perm_b32 v69, v70, v69, s2
	v_perm_b32 v66, v240, v138, s42
	v_perm_b32 v67, v240, v138, s43
	v_perm_b32 v68, v240, v139, s42
	v_or_b32_e32 v69, 0x64006400, v69
	v_pk_add_f16 v66, v66, s3 op_sel_hi:[1,0]
	v_pk_add_f16 v67, v67, s3 op_sel_hi:[1,0]
	v_pk_add_f16 v68, v68, s3 op_sel_hi:[1,0]
	v_pk_add_f16 v69, v69, s3 op_sel_hi:[1,0]
	s_nop 1
	v_mfma_f32_32x32x16_f16 v[0:15], v[52:55], v[66:69], v[0:15]
	v_perm_b32 v48, v240, v136, s42
	v_perm_b32 v49, v240, v136, s43
	v_perm_b32 v50, v240, v137, s42
	v_perm_b32 v51, v240, v137, s43
	v_pk_add_f16 v48, v48, s3 op_sel_hi:[1,0]
	v_pk_add_f16 v49, v49, s3 op_sel_hi:[1,0]
	v_pk_add_f16 v50, v50, s3 op_sel_hi:[1,0]
	v_pk_add_f16 v51, v51, s3 op_sel_hi:[1,0]
	v_cvt_pk_f16_f32 v39, v38, v39
	v_cvt_pk_f16_f32 v38, v36, v37
	v_mfma_f32_32x32x16_f16 v[16:31], v[52:55], v[48:51], v[16:31]
	v_perm_b32 v48, v240, v134, s42
	v_perm_b32 v49, v240, v134, s43
	v_perm_b32 v50, v240, v135, s42
	v_perm_b32 v51, v240, v135, s43
	v_pk_add_f16 v48, v48, s3 op_sel_hi:[1,0]
	v_pk_add_f16 v49, v49, s3 op_sel_hi:[1,0]
	v_pk_add_f16 v50, v50, s3 op_sel_hi:[1,0]
	v_pk_add_f16 v51, v51, s3 op_sel_hi:[1,0]
	v_cvt_pk_f16_f32 v55, v62, v63
	v_cvt_pk_f16_f32 v54, v60, v61
	v_cvt_pk_f16_f32 v53, v58, v59
	v_cvt_pk_f16_f32 v52, v56, v57
	s_waitcnt vmcnt(2)
	v_cvt_pk_f16_f32 v37, v34, v35
	v_mfma_f32_32x32x16_f16 v[0:15], v[52:55], v[48:51], v[0:15]
	v_perm_b32 v48, v240, v142, s42
	v_perm_b32 v49, v240, v142, s43
	v_perm_b32 v50, v240, v143, s42
	v_perm_b32 v51, v240, v143, s43
	v_pk_add_f16 v48, v48, s3 op_sel_hi:[1,0]
	v_pk_add_f16 v49, v49, s3 op_sel_hi:[1,0]
	v_pk_add_f16 v50, v50, s3 op_sel_hi:[1,0]
	v_pk_add_f16 v51, v51, s3 op_sel_hi:[1,0]
	v_cvt_pk_f16_f32 v36, v32, v33
	s_waitcnt vmcnt(1)
	v_mfma_f32_32x32x16_f16 v[16:31], v[52:55], v[48:51], v[16:31]
	v_lshrrev_b32_e32 v51, 16, v133
	v_lshrrev_b32_e32 v52, 8, v133
	v_perm_b32 v51, v52, v51, s2
	v_perm_b32 v48, v240, v132, s42
	v_perm_b32 v49, v240, v132, s43
	v_perm_b32 v50, v240, v133, s42
	v_or_b32_e32 v51, 0x64006400, v51
	v_pk_add_f16 v48, v48, s3 op_sel_hi:[1,0]
	v_pk_add_f16 v49, v49, s3 op_sel_hi:[1,0]
	v_pk_add_f16 v50, v50, s3 op_sel_hi:[1,0]
	v_pk_add_f16 v51, v51, s3 op_sel_hi:[1,0]
	s_nop 1
	v_mfma_f32_32x32x16_f16 v[0:15], v[36:39], v[48:51], v[0:15]
	v_perm_b32 v32, v240, v140, s42
	v_perm_b32 v33, v240, v140, s43
	v_perm_b32 v34, v240, v141, s42
	v_perm_b32 v35, v240, v141, s43
	v_pk_add_f16 v32, v32, s3 op_sel_hi:[1,0]
	v_pk_add_f16 v33, v33, s3 op_sel_hi:[1,0]
	v_pk_add_f16 v34, v34, s3 op_sel_hi:[1,0]
	v_pk_add_f16 v35, v35, s3 op_sel_hi:[1,0]
	s_nop 1
	v_mfma_f32_32x32x16_f16 v[16:31], v[36:39], v[32:35], v[16:31]
	v_perm_b32 v32, v240, v130, s42
	v_perm_b32 v33, v240, v130, s43
	v_perm_b32 v34, v240, v131, s42
	v_perm_b32 v35, v240, v131, s43
	v_pk_add_f16 v32, v32, s3 op_sel_hi:[1,0]
	v_pk_add_f16 v33, v33, s3 op_sel_hi:[1,0]
	v_pk_add_f16 v34, v34, s3 op_sel_hi:[1,0]
	v_pk_add_f16 v35, v35, s3 op_sel_hi:[1,0]
	v_cvt_pk_f16_f32 v39, v46, v47
	v_cvt_pk_f16_f32 v38, v44, v45
	v_cvt_pk_f16_f32 v37, v42, v43
	v_cvt_pk_f16_f32 v36, v40, v41
	s_waitcnt vmcnt(0)
	s_nop 0
	v_mfma_f32_32x32x16_f16 v[0:15], v[36:39], v[32:35], v[0:15]
	v_perm_b32 v32, v240, v64, s42
	v_perm_b32 v33, v240, v64, s43
	v_perm_b32 v34, v240, v65, s42
	v_perm_b32 v35, v240, v65, s43
	v_pk_add_f16 v32, v32, s3 op_sel_hi:[1,0]
	v_pk_add_f16 v33, v33, s3 op_sel_hi:[1,0]
	v_pk_add_f16 v34, v34, s3 op_sel_hi:[1,0]
	v_pk_add_f16 v35, v35, s3 op_sel_hi:[1,0]
	s_nop 3
	v_mfma_f32_32x32x16_f16 v[16:31], v[36:39], v[32:35], v[16:31]
	s_nop 7
	s_nop 4
	v_cvt_pk_f16_f32 v254, v0, v1
	v_cvt_pk_f16_f32 v255, v2, v3
	ds_write_b64 v251, v[254:255] offset:18432
	v_pk_add_f32 v[222:223], v[222:223], v[0:1]
	v_pk_fma_f32 v[194:195], v[0:1], v[0:1], v[194:195]
	v_pk_add_f32 v[220:221], v[220:221], v[2:3]
	v_pk_fma_f32 v[192:193], v[2:3], v[2:3], v[192:193]
	v_cvt_pk_f16_f32 v252, v4, v5
	v_cvt_pk_f16_f32 v253, v6, v7
	ds_write_b64 v251, v[252:253] offset:18448
	v_pk_add_f32 v[218:219], v[218:219], v[4:5]
	v_pk_fma_f32 v[184:185], v[4:5], v[4:5], v[184:185]
	v_pk_add_f32 v[216:217], v[216:217], v[6:7]
	v_pk_fma_f32 v[166:167], v[6:7], v[6:7], v[166:167]
	v_cvt_pk_f16_f32 v254, v8, v9
	v_cvt_pk_f16_f32 v255, v10, v11
	ds_write_b64 v251, v[254:255] offset:18464
	v_pk_add_f32 v[214:215], v[214:215], v[8:9]
	v_pk_fma_f32 v[164:165], v[8:9], v[8:9], v[164:165]
	v_pk_add_f32 v[204:205], v[204:205], v[10:11]
	v_pk_fma_f32 v[162:163], v[10:11], v[10:11], v[162:163]
	v_cvt_pk_f16_f32 v252, v12, v13
	v_cvt_pk_f16_f32 v253, v14, v15
	ds_write_b64 v251, v[252:253] offset:18480
	v_pk_add_f32 v[202:203], v[202:203], v[12:13]
	v_pk_fma_f32 v[160:161], v[12:13], v[12:13], v[160:161]
	v_pk_add_f32 v[196:197], v[196:197], v[14:15]
	v_pk_fma_f32 v[156:157], v[14:15], v[14:15], v[156:157]
	v_cvt_pk_f16_f32 v254, v16, v17
	v_cvt_pk_f16_f32 v255, v18, v19
	ds_write_b64 v251, v[254:255] offset:23040
	v_pk_add_f32 v[222:223], v[222:223], v[16:17]
	v_pk_fma_f32 v[194:195], v[16:17], v[16:17], v[194:195]
	v_pk_add_f32 v[220:221], v[220:221], v[18:19]
	v_pk_fma_f32 v[192:193], v[18:19], v[18:19], v[192:193]
	v_cvt_pk_f16_f32 v252, v20, v21
	v_cvt_pk_f16_f32 v253, v22, v23
	ds_write_b64 v251, v[252:253] offset:23056
	v_pk_add_f32 v[218:219], v[218:219], v[20:21]
	v_pk_fma_f32 v[184:185], v[20:21], v[20:21], v[184:185]
	v_pk_add_f32 v[216:217], v[216:217], v[22:23]
	v_pk_fma_f32 v[166:167], v[22:23], v[22:23], v[166:167]
	v_cvt_pk_f16_f32 v254, v24, v25
	v_cvt_pk_f16_f32 v255, v26, v27
	ds_write_b64 v251, v[254:255] offset:23072
	v_pk_add_f32 v[214:215], v[214:215], v[24:25]
	v_pk_fma_f32 v[164:165], v[24:25], v[24:25], v[164:165]
	v_pk_add_f32 v[204:205], v[204:205], v[26:27]
	v_pk_fma_f32 v[162:163], v[26:27], v[26:27], v[162:163]
	v_cvt_pk_f16_f32 v252, v28, v29
	v_cvt_pk_f16_f32 v253, v30, v31
	ds_write_b64 v251, v[252:253] offset:23088
	v_pk_add_f32 v[202:203], v[202:203], v[28:29]
	v_pk_fma_f32 v[160:161], v[28:29], v[28:29], v[160:161]
	v_pk_add_f32 v[196:197], v[196:197], v[30:31]
	v_pk_fma_f32 v[156:157], v[30:31], v[30:31], v[156:157]
	s_nop 4
	s_nop 0
	v_add_f32_dpp v222, v222, v222 row_half_mirror row_mask:0xf bank_mask:0x5
	v_add_f32_dpp v222, v223, v223 row_half_mirror row_mask:0xf bank_mask:0xa
	v_add_f32_dpp v220, v220, v220 row_half_mirror row_mask:0xf bank_mask:0x5
	v_add_f32_dpp v220, v221, v221 row_half_mirror row_mask:0xf bank_mask:0xa
	v_add_f32_dpp v218, v218, v218 row_half_mirror row_mask:0xf bank_mask:0x5
	v_add_f32_dpp v218, v219, v219 row_half_mirror row_mask:0xf bank_mask:0xa
	v_add_f32_dpp v216, v216, v216 row_half_mirror row_mask:0xf bank_mask:0x5
	v_add_f32_dpp v216, v217, v217 row_half_mirror row_mask:0xf bank_mask:0xa
	v_add_f32_dpp v214, v214, v214 row_half_mirror row_mask:0xf bank_mask:0x5
	v_add_f32_dpp v214, v215, v215 row_half_mirror row_mask:0xf bank_mask:0xa
	v_add_f32_dpp v204, v204, v204 row_half_mirror row_mask:0xf bank_mask:0x5
	v_add_f32_dpp v204, v205, v205 row_half_mirror row_mask:0xf bank_mask:0xa
	v_add_f32_dpp v202, v202, v202 row_half_mirror row_mask:0xf bank_mask:0x5
	v_add_f32_dpp v202, v203, v203 row_half_mirror row_mask:0xf bank_mask:0xa
	v_add_f32_dpp v196, v196, v196 row_half_mirror row_mask:0xf bank_mask:0x5
	v_add_f32_dpp v196, v197, v197 row_half_mirror row_mask:0xf bank_mask:0xa
	v_add_f32_dpp v194, v194, v194 row_half_mirror row_mask:0xf bank_mask:0x5
	v_add_f32_dpp v194, v195, v195 row_half_mirror row_mask:0xf bank_mask:0xa
	v_add_f32_dpp v192, v192, v192 row_half_mirror row_mask:0xf bank_mask:0x5
	v_add_f32_dpp v192, v193, v193 row_half_mirror row_mask:0xf bank_mask:0xa
	v_add_f32_dpp v184, v184, v184 row_half_mirror row_mask:0xf bank_mask:0x5
	v_add_f32_dpp v184, v185, v185 row_half_mirror row_mask:0xf bank_mask:0xa
	v_add_f32_dpp v166, v166, v166 row_half_mirror row_mask:0xf bank_mask:0x5
	v_add_f32_dpp v166, v167, v167 row_half_mirror row_mask:0xf bank_mask:0xa
	v_add_f32_dpp v164, v164, v164 row_half_mirror row_mask:0xf bank_mask:0x5
	v_add_f32_dpp v164, v165, v165 row_half_mirror row_mask:0xf bank_mask:0xa
	v_add_f32_dpp v162, v162, v162 row_half_mirror row_mask:0xf bank_mask:0x5
	v_add_f32_dpp v162, v163, v163 row_half_mirror row_mask:0xf bank_mask:0xa
	v_add_f32_dpp v160, v160, v160 row_half_mirror row_mask:0xf bank_mask:0x5
	v_add_f32_dpp v160, v161, v161 row_half_mirror row_mask:0xf bank_mask:0xa
	v_add_f32_dpp v156, v156, v156 row_half_mirror row_mask:0xf bank_mask:0x5
	v_add_f32_dpp v156, v157, v157 row_half_mirror row_mask:0xf bank_mask:0xa
	v_add_f32_dpp v222, v222, v222 row_ror:8 row_mask:0xf bank_mask:0x3
	v_add_f32_dpp v222, v220, v220 row_ror:8 row_mask:0xf bank_mask:0xc
	v_add_f32_dpp v218, v218, v218 row_ror:8 row_mask:0xf bank_mask:0x3
	v_add_f32_dpp v218, v216, v216 row_ror:8 row_mask:0xf bank_mask:0xc
	v_add_f32_dpp v214, v214, v214 row_ror:8 row_mask:0xf bank_mask:0x3
	v_add_f32_dpp v214, v204, v204 row_ror:8 row_mask:0xf bank_mask:0xc
	v_add_f32_dpp v202, v202, v202 row_ror:8 row_mask:0xf bank_mask:0x3
	v_add_f32_dpp v202, v196, v196 row_ror:8 row_mask:0xf bank_mask:0xc
	v_add_f32_dpp v194, v194, v194 row_ror:8 row_mask:0xf bank_mask:0x3
	v_add_f32_dpp v194, v192, v192 row_ror:8 row_mask:0xf bank_mask:0xc
	v_add_f32_dpp v184, v184, v184 row_ror:8 row_mask:0xf bank_mask:0x3
	v_add_f32_dpp v184, v166, v166 row_ror:8 row_mask:0xf bank_mask:0xc
	v_add_f32_dpp v164, v164, v164 row_ror:8 row_mask:0xf bank_mask:0x3
	v_add_f32_dpp v164, v162, v162 row_ror:8 row_mask:0xf bank_mask:0xc
	v_add_f32_dpp v160, v160, v160 row_ror:8 row_mask:0xf bank_mask:0x3
	v_add_f32_dpp v160, v156, v156 row_ror:8 row_mask:0xf bank_mask:0xc
	v_add_f32_dpp v222, v222, v222 quad_perm:[1,0,3,2] row_mask:0xf bank_mask:0xf
	v_add_f32_dpp v218, v218, v218 quad_perm:[1,0,3,2] row_mask:0xf bank_mask:0xf
	v_add_f32_dpp v214, v214, v214 quad_perm:[1,0,3,2] row_mask:0xf bank_mask:0xf
	v_add_f32_dpp v202, v202, v202 quad_perm:[1,0,3,2] row_mask:0xf bank_mask:0xf
	v_add_f32_dpp v194, v194, v194 quad_perm:[1,0,3,2] row_mask:0xf bank_mask:0xf
	v_add_f32_dpp v184, v184, v184 quad_perm:[1,0,3,2] row_mask:0xf bank_mask:0xf
	v_add_f32_dpp v164, v164, v164 quad_perm:[1,0,3,2] row_mask:0xf bank_mask:0xf
	v_add_f32_dpp v160, v160, v160 quad_perm:[1,0,3,2] row_mask:0xf bank_mask:0xf
	v_add_f32_dpp v222, v222, v222 quad_perm:[2,3,0,1] row_mask:0xf bank_mask:0xf
	v_add_f32_dpp v218, v218, v218 quad_perm:[2,3,0,1] row_mask:0xf bank_mask:0xf
	v_add_f32_dpp v214, v214, v214 quad_perm:[2,3,0,1] row_mask:0xf bank_mask:0xf
	v_add_f32_dpp v202, v202, v202 quad_perm:[2,3,0,1] row_mask:0xf bank_mask:0xf
	v_add_f32_dpp v194, v194, v194 quad_perm:[2,3,0,1] row_mask:0xf bank_mask:0xf
	v_add_f32_dpp v184, v184, v184 quad_perm:[2,3,0,1] row_mask:0xf bank_mask:0xf
	v_add_f32_dpp v164, v164, v164 quad_perm:[2,3,0,1] row_mask:0xf bank_mask:0xf
	v_add_f32_dpp v160, v160, v160 quad_perm:[2,3,0,1] row_mask:0xf bank_mask:0xf
	s_mov_b32 exec_lo, 0x11111111
	s_mov_b32 exec_hi, 0x11111111
	ds_add_f32 v250, v222 offset:0
	ds_add_f32 v250, v218 offset:32
	ds_add_f32 v250, v214 offset:64
	ds_add_f32 v250, v202 offset:96
	ds_add_f32 v250, v194 offset:256
	ds_add_f32 v250, v184 offset:288
	ds_add_f32 v250, v164 offset:320
	ds_add_f32 v250, v160 offset:352
	s_mov_b64 exec, -1
	s_waitcnt lgkmcnt(0)
	s_barrier
